# router logits block: weight ds_reads software-pipelined 7 deep using the VGPRs of the precomputed LDS addresses (same fma order)
# speedup vs baseline: 1.0881x; 1.0156x over previous
.LBB0_758:
	s_or_b64 exec, exec, s[2:3]
	v_readlane_b32 s2, v254, 32
	v_readlane_b32 s3, v254, 33
	s_lshl_b32 s36, s2, 5
	v_readlane_b32 s2, v254, 37
	v_writelane_b32 v254, s75, 48
	s_lshr_b32 s5, s78, 1
	v_readlane_b32 s3, v254, 34
	s_lshl_b32 s3, s3, 3
	s_abs_i32 s4, s3
	v_cvt_f32_u32_e32 v0, s4
	s_sub_i32 s7, 0, s4
	s_add_i32 s6, s5, s3
	s_add_i32 s6, s6, -1
	v_rcp_iflag_f32_e32 v0, v0
	s_xor_b32 s3, s6, s3
	s_abs_i32 s6, s6
	s_lshl_b32 s2, s2, 3
	v_mul_f32_e32 v0, 0x4f7ffffe, v0
	v_cvt_u32_f32_e32 v0, v0
	s_add_i32 s2, s2, s75
	s_ashr_i32 s3, s3, 31
	v_writelane_b32 v254, s78, 49
	v_readfirstlane_b32 s9, v0
	s_mul_i32 s7, s7, s9
	s_mul_hi_u32 s7, s9, s7
	s_add_i32 s9, s9, s7
	s_mul_hi_u32 s7, s6, s9
	s_mul_i32 s9, s7, s4
	s_sub_i32 s6, s6, s9
	s_add_i32 s9, s7, 1
	s_sub_i32 s10, s6, s4
	s_cmp_ge_u32 s6, s4
	s_cselect_b32 s7, s9, s7
	s_cselect_b32 s6, s10, s6
	s_add_i32 s9, s7, 1
	s_cmp_ge_u32 s6, s4
	s_cselect_b32 s4, s9, s7
	s_xor_b32 s4, s4, s3
	s_sub_i32 s4, s4, s3
	s_mul_i32 s3, s4, s2
	s_add_i32 s2, s3, s4
	s_min_i32 s90, s5, s2
	s_cmp_lt_i32 s3, s90
	s_waitcnt lgkmcnt(0)
	s_barrier
	s_cbranch_scc0 .LBB0_779
	s_load_dwordx2 s[0:1], s[0:1], 0xe0
	v_readlane_b32 s2, v254, 48
	s_lshl_b32 s2, s2, 9
	v_lshrrev_b32_e32 v0, 1, v8
	s_add_i32 s4, s91, s2
	v_and_or_b32 v200, v0, 31, s36
	s_add_i32 s4, s4, 0x20000
	v_readlane_b32 s62, v254, 39
	s_waitcnt lgkmcnt(0)
	v_lshl_add_u64 v[0:1], v[200:201], 2, s[0:1]
	v_readlane_b32 s63, v254, 40
	s_add_u32 s0, s62, 0x36000000
	s_addc_u32 s1, s63, 0
	s_add_u32 s60, s62, 0x5c400000
	s_addc_u32 s61, s63, 0
	s_add_i32 s2, s91, 0x22000
	s_add_u32 s5, s62, 0x9f500000
	v_writelane_b32 v254, s5, 53
	s_addc_u32 s5, s63, 0
	s_add_u32 s6, s62, 0x9d000000
	v_writelane_b32 v254, s5, 54
	s_addc_u32 s7, s63, 0
	v_writelane_b32 v254, s6, 45
	v_and_b32_e32 v90, 63, v8
	global_load_dword v122, v[0:1], off
	v_writelane_b32 v254, s7, 46
	s_add_u32 s6, s62, 0x9d100000
	s_addc_u32 s7, s63, 0
	s_lshl_b32 s96, s3, 1
	v_writelane_b32 v254, s6, 43
	s_ashr_i32 s97, s96, 31
	v_lshlrev_b32_e32 v0, 5, v90
	v_writelane_b32 v254, s7, 44
	s_lshl_b64 s[6:7], s[96:97], 11
	s_add_u32 s10, s0, s6
	s_addc_u32 s11, s1, s7
	s_add_u32 s6, s60, s6
	s_addc_u32 s7, s61, s7
	global_load_dwordx4 v[68:71], v0, s[10:11] offset:16
	global_load_dwordx4 v[76:79], v0, s[10:11]
	global_load_dwordx4 v[64:67], v0, s[6:7] offset:16
	global_load_dwordx4 v[72:75], v0, s[6:7]
	s_or_b32 s6, s96, 1
	s_ashr_i32 s7, s6, 31
	s_lshl_b64 s[6:7], s[6:7], 11
	s_add_u32 s10, s0, s6
	s_addc_u32 s11, s1, s7
	s_add_u32 s6, s60, s6
	s_addc_u32 s7, s61, s7
	global_load_dwordx4 v[52:55], v0, s[10:11] offset:16
	global_load_dwordx4 v[60:63], v0, s[10:11]
	global_load_dwordx4 v[48:51], v0, s[6:7] offset:16
	global_load_dwordx4 v[56:59], v0, s[6:7]
	v_and_b32_e32 v2, 16, v8
	v_cmp_eq_u32_e64 s[10:11], 0, v2
	v_and_b32_e32 v2, 8, v8
	v_cmp_eq_u32_e64 s[12:13], 0, v2
	v_and_b32_e32 v2, 4, v8
	v_mov_b32_e32 v1, v201
	v_cmp_eq_u32_e64 s[14:15], 0, v2
	v_and_b32_e32 v2, 2, v8
	v_lshlrev_b32_e32 v200, 4, v90
	v_cmp_eq_u32_e64 s[16:17], 0, v2
	v_bfe_u32 v126, v8, 1, 5
	v_and_b32_e32 v2, 1, v8
	v_lshl_add_u64 v[82:83], s[0:1], 0, v[0:1]
	v_lshl_add_u64 v[84:85], s[60:61], 0, v[0:1]
	v_lshl_add_u64 v[0:1], s[62:63], 0, v[0:1]
	s_mov_b64 s[0:1], 0x3e800000
	v_add_u32_e32 v125, s91, v200
	v_cmp_eq_u32_e64 s[18:19], 0, v2
	v_cmp_eq_u32_e32 vcc, 1, v2
	v_lshlrev_b32_e32 v2, 2, v126
	v_lshl_add_u64 v[86:87], v[0:1], 0, s[0:1]
	v_lshl_add_u64 v[0:1], s[62:63], 0, v[200:201]
	s_mov_b64 s[0:1], 0x60800000
	v_add_u32_e32 v123, s8, v200
	v_add_u32_e32 v124, s2, v200
	v_cmp_eq_u32_e64 s[6:7], 0, v90
	v_cmp_gt_u32_e64 s[8:9], 32, v90
	v_add_u32_e32 v127, s4, v2
	v_cmp_lt_u32_e64 s[20:21], 1, v90
	v_cmp_lt_u32_e64 s[22:23], 3, v90
	v_cmp_lt_u32_e64 s[24:25], 5, v90
	v_cmp_lt_u32_e64 s[26:27], 7, v90
	v_cmp_lt_u32_e64 s[28:29], 9, v90
	v_cmp_lt_u32_e64 s[30:31], 11, v90
	v_cmp_lt_u32_e64 s[34:35], 13, v90
	v_cmp_lt_u32_e64 s[38:39], 15, v90
	v_cmp_lt_u32_e64 s[40:41], 17, v90
	v_cmp_lt_u32_e64 s[42:43], 19, v90
	v_cmp_lt_u32_e64 s[44:45], 21, v90
	v_cmp_lt_u32_e64 s[46:47], 23, v90
	v_cmp_lt_u32_e64 s[48:49], 25, v90
	v_cmp_lt_u32_e64 s[50:51], 27, v90
	v_cmp_lt_u32_e64 s[86:87], 29, v90
	v_cmp_lt_u32_e64 s[52:53], 31, v90
	v_cmp_lt_u32_e64 s[54:55], 33, v90
	v_cmp_lt_u32_e64 s[56:57], 35, v90
	v_cmp_lt_u32_e64 s[58:59], 37, v90
	v_cmp_lt_u32_e64 s[60:61], 39, v90
	v_add_u32_e32 v128, s33, v2
	v_add_u32_e32 v129, 0x10000, v125
	v_lshl_add_u64 v[88:89], v[0:1], 0, s[0:1]
	s_mov_b32 s5, -1
	v_lshlrev_b32_e32 v200, 2, v200
	s_xor_b64 s[0:1], vcc, -1
	v_cmp_lt_u32_e64 s[62:63], 41, v90
	v_cmp_lt_u32_e64 s[64:65], 43, v90
	v_cmp_lt_u32_e64 s[66:67], 45, v90
	v_cmp_lt_u32_e64 s[68:69], 47, v90
	v_cmp_lt_u32_e64 s[70:71], 49, v90
	v_cmp_lt_u32_e64 s[72:73], 51, v90
	v_cmp_lt_u32_e64 s[74:75], 53, v90
	v_cmp_lt_u32_e64 s[76:77], 55, v90
	v_cmp_lt_u32_e64 s[78:79], 57, v90
	v_cmp_lt_u32_e64 s[80:81], 59, v90
	v_cmp_eq_u32_e64 s[82:83], 31, v126
	s_branch .LBB0_761

.LBB0_767:
	s_or_b64 exec, exec, s[84:85]
	s_add_i32 s2, s3, 1
	s_cmp_ge_i32 s2, s90
	s_cselect_b64 s[88:89], -1, 0
	s_cmp_lt_i32 s2, s90
	s_cselect_b32 s3, s2, s3
	s_lshl_b32 s84, s3, 1
	s_ashr_i32 s85, s84, 31
	s_lshl_b64 s[92:93], s[84:85], 11
	s_or_b32 s84, s84, 1
	s_ashr_i32 s85, s84, 31
	v_lshl_add_u64 v[48:49], v[82:83], 0, s[92:93]
	s_lshl_b64 s[84:85], s[84:85], 11
	v_lshl_add_u64 v[50:51], v[84:85], 0, s[92:93]
	global_load_dwordx4 v[68:71], v[48:49], off offset:16
	global_load_dwordx4 v[76:79], v[48:49], off
	global_load_dwordx4 v[64:67], v[50:51], off offset:16
	global_load_dwordx4 v[72:75], v[50:51], off
	v_lshl_add_u64 v[48:49], v[82:83], 0, s[84:85]
	v_lshl_add_u64 v[56:57], v[84:85], 0, s[84:85]
	global_load_dwordx4 v[52:55], v[48:49], off offset:16
	global_load_dwordx4 v[60:63], v[48:49], off
	s_nop 0
	global_load_dwordx4 v[48:51], v[56:57], off offset:16
	s_nop 0
	global_load_dwordx4 v[56:59], v[56:57], off
	s_waitcnt lgkmcnt(0)
	ds_read_b128 v[130:133], v125
	ds_read_b128 v[134:137], v125 offset:1024
	ds_read_b128 v[138:141], v125 offset:2048
	ds_read_b128 v[142:145], v125 offset:3072
	ds_read_b128 v[146:149], v125 offset:4096
	ds_read_b128 v[150:153], v125 offset:5120
	ds_read_b128 v[154:157], v125 offset:6144
	ds_read_b128 v[158:161], v125 offset:7168
	s_waitcnt lgkmcnt(7)
	v_pk_fma_f32 v[162:163], v[104:105], v[130:131], 0 op_sel_hi:[1,1,0]
	v_pk_fma_f32 v[164:165], v[120:121], v[130:131], 0 op_sel_hi:[1,1,0]
	v_pk_fma_f32 v[162:163], v[102:103], v[132:133], v[162:163]
	v_pk_fma_f32 v[164:165], v[118:119], v[132:133], v[164:165]
	ds_read_b128 v[130:133], v125 offset:8192
	s_waitcnt lgkmcnt(7)
	v_pk_fma_f32 v[162:163], v[100:101], v[134:135], v[162:163]
	v_pk_fma_f32 v[164:165], v[116:117], v[134:135], v[164:165]
	v_pk_fma_f32 v[162:163], v[98:99], v[136:137], v[162:163]
	v_pk_fma_f32 v[164:165], v[114:115], v[136:137], v[164:165]
	ds_read_b128 v[134:137], v125 offset:9216
	s_waitcnt lgkmcnt(7)
	v_pk_fma_f32 v[162:163], v[96:97], v[138:139], v[162:163]
	v_pk_fma_f32 v[164:165], v[112:113], v[138:139], v[164:165]
	v_pk_fma_f32 v[162:163], v[94:95], v[140:141], v[162:163]
	v_pk_fma_f32 v[164:165], v[110:111], v[140:141], v[164:165]
	ds_read_b128 v[138:141], v125 offset:10240
	s_waitcnt lgkmcnt(7)
	v_pk_fma_f32 v[162:163], v[92:93], v[142:143], v[162:163]
	v_pk_fma_f32 v[164:165], v[108:109], v[142:143], v[164:165]
	v_pk_fma_f32 v[162:163], v[90:91], v[144:145], v[162:163]
	v_pk_fma_f32 v[164:165], v[106:107], v[144:145], v[164:165]
	v_add_f32_e32 v178, v162, v163
	v_add_f32_e32 v175, v164, v165
	ds_read_b128 v[142:145], v125 offset:11264
	s_waitcnt lgkmcnt(7)
	v_pk_fma_f32 v[162:163], v[104:105], v[146:147], 0 op_sel_hi:[1,1,0]
	v_pk_fma_f32 v[164:165], v[120:121], v[146:147], 0 op_sel_hi:[1,1,0]
	v_pk_fma_f32 v[162:163], v[102:103], v[148:149], v[162:163]
	v_pk_fma_f32 v[164:165], v[118:119], v[148:149], v[164:165]
	ds_read_b128 v[146:149], v125 offset:12288
	s_waitcnt lgkmcnt(7)
	v_pk_fma_f32 v[162:163], v[100:101], v[150:151], v[162:163]
	v_pk_fma_f32 v[164:165], v[116:117], v[150:151], v[164:165]
	v_pk_fma_f32 v[162:163], v[98:99], v[152:153], v[162:163]
	v_pk_fma_f32 v[164:165], v[114:115], v[152:153], v[164:165]
	ds_read_b128 v[150:153], v125 offset:13312
	s_waitcnt lgkmcnt(7)
	v_pk_fma_f32 v[162:163], v[96:97], v[154:155], v[162:163]
	v_pk_fma_f32 v[164:165], v[112:113], v[154:155], v[164:165]
	v_pk_fma_f32 v[162:163], v[94:95], v[156:157], v[162:163]
	v_pk_fma_f32 v[164:165], v[110:111], v[156:157], v[164:165]
	ds_read_b128 v[154:157], v125 offset:14336
	s_waitcnt lgkmcnt(7)
	v_pk_fma_f32 v[162:163], v[92:93], v[158:159], v[162:163]
	v_pk_fma_f32 v[164:165], v[108:109], v[158:159], v[164:165]
	v_pk_fma_f32 v[162:163], v[90:91], v[160:161], v[162:163]
	v_pk_fma_f32 v[164:165], v[106:107], v[160:161], v[164:165]
	v_add_f32_e32 v180, v162, v163
	v_add_f32_e32 v176, v164, v165
	ds_read_b128 v[158:161], v125 offset:15360
	s_waitcnt lgkmcnt(7)
	v_pk_fma_f32 v[162:163], v[104:105], v[130:131], 0 op_sel_hi:[1,1,0]
	v_pk_fma_f32 v[164:165], v[120:121], v[130:131], 0 op_sel_hi:[1,1,0]
	v_pk_fma_f32 v[162:163], v[102:103], v[132:133], v[162:163]
	v_pk_fma_f32 v[164:165], v[118:119], v[132:133], v[164:165]
	ds_read_b128 v[130:133], v125 offset:16384
	s_waitcnt lgkmcnt(7)
	v_pk_fma_f32 v[162:163], v[100:101], v[134:135], v[162:163]
	v_pk_fma_f32 v[164:165], v[116:117], v[134:135], v[164:165]
	v_pk_fma_f32 v[162:163], v[98:99], v[136:137], v[162:163]
	v_pk_fma_f32 v[164:165], v[114:115], v[136:137], v[164:165]
	ds_read_b128 v[134:137], v125 offset:17408
	s_waitcnt lgkmcnt(7)
	v_pk_fma_f32 v[162:163], v[96:97], v[138:139], v[162:163]
	v_pk_fma_f32 v[164:165], v[112:113], v[138:139], v[164:165]
	v_pk_fma_f32 v[162:163], v[94:95], v[140:141], v[162:163]
	v_pk_fma_f32 v[164:165], v[110:111], v[140:141], v[164:165]
	ds_read_b128 v[138:141], v125 offset:18432
	s_waitcnt lgkmcnt(7)
	v_pk_fma_f32 v[162:163], v[92:93], v[142:143], v[162:163]
	v_pk_fma_f32 v[164:165], v[108:109], v[142:143], v[164:165]
	v_pk_fma_f32 v[162:163], v[90:91], v[144:145], v[162:163]
	v_pk_fma_f32 v[164:165], v[106:107], v[144:145], v[164:165]
	v_add_f32_e32 v182, v162, v163
	v_add_f32_e32 v177, v164, v165
	ds_read_b128 v[142:145], v125 offset:19456
	s_waitcnt lgkmcnt(7)
	v_pk_fma_f32 v[162:163], v[104:105], v[146:147], 0 op_sel_hi:[1,1,0]
	v_pk_fma_f32 v[164:165], v[120:121], v[146:147], 0 op_sel_hi:[1,1,0]
	v_pk_fma_f32 v[162:163], v[102:103], v[148:149], v[162:163]
	v_pk_fma_f32 v[164:165], v[118:119], v[148:149], v[164:165]
	ds_read_b128 v[146:149], v125 offset:20480
	s_waitcnt lgkmcnt(7)
	v_pk_fma_f32 v[162:163], v[100:101], v[150:151], v[162:163]
	v_pk_fma_f32 v[164:165], v[116:117], v[150:151], v[164:165]
	v_pk_fma_f32 v[162:163], v[98:99], v[152:153], v[162:163]
	v_pk_fma_f32 v[164:165], v[114:115], v[152:153], v[164:165]
	ds_read_b128 v[150:153], v125 offset:21504
	s_waitcnt lgkmcnt(7)
	v_pk_fma_f32 v[162:163], v[96:97], v[154:155], v[162:163]
	v_pk_fma_f32 v[164:165], v[112:113], v[154:155], v[164:165]
	v_pk_fma_f32 v[162:163], v[94:95], v[156:157], v[162:163]
	v_pk_fma_f32 v[164:165], v[110:111], v[156:157], v[164:165]
	ds_read_b128 v[154:157], v125 offset:22528
	s_waitcnt lgkmcnt(7)
	v_pk_fma_f32 v[162:163], v[92:93], v[158:159], v[162:163]
	v_pk_fma_f32 v[164:165], v[108:109], v[158:159], v[164:165]
	v_pk_fma_f32 v[162:163], v[90:91], v[160:161], v[162:163]
	v_pk_fma_f32 v[164:165], v[106:107], v[160:161], v[164:165]
	v_add_f32_e32 v184, v162, v163
	v_add_f32_e32 v179, v164, v165
	ds_read_b128 v[158:161], v125 offset:23552
	s_waitcnt lgkmcnt(7)
	v_pk_fma_f32 v[162:163], v[104:105], v[130:131], 0 op_sel_hi:[1,1,0]
	v_pk_fma_f32 v[164:165], v[120:121], v[130:131], 0 op_sel_hi:[1,1,0]
	v_pk_fma_f32 v[162:163], v[102:103], v[132:133], v[162:163]
	v_pk_fma_f32 v[164:165], v[118:119], v[132:133], v[164:165]
	ds_read_b128 v[130:133], v125 offset:24576
	s_waitcnt lgkmcnt(7)
	v_pk_fma_f32 v[162:163], v[100:101], v[134:135], v[162:163]
	v_pk_fma_f32 v[164:165], v[116:117], v[134:135], v[164:165]
	v_pk_fma_f32 v[162:163], v[98:99], v[136:137], v[162:163]
	v_pk_fma_f32 v[164:165], v[114:115], v[136:137], v[164:165]
	ds_read_b128 v[134:137], v125 offset:25600
	s_waitcnt lgkmcnt(7)
	v_pk_fma_f32 v[162:163], v[96:97], v[138:139], v[162:163]
	v_pk_fma_f32 v[164:165], v[112:113], v[138:139], v[164:165]
	v_pk_fma_f32 v[162:163], v[94:95], v[140:141], v[162:163]
	v_pk_fma_f32 v[164:165], v[110:111], v[140:141], v[164:165]
	ds_read_b128 v[138:141], v125 offset:26624
	s_waitcnt lgkmcnt(7)
	v_pk_fma_f32 v[162:163], v[92:93], v[142:143], v[162:163]
	v_pk_fma_f32 v[164:165], v[108:109], v[142:143], v[164:165]
	v_pk_fma_f32 v[162:163], v[90:91], v[144:145], v[162:163]
	v_pk_fma_f32 v[164:165], v[106:107], v[144:145], v[164:165]
	v_add_f32_e32 v186, v162, v163
	v_add_f32_e32 v181, v164, v165
	ds_read_b128 v[142:145], v125 offset:27648
	s_waitcnt lgkmcnt(7)
	v_pk_fma_f32 v[162:163], v[104:105], v[146:147], 0 op_sel_hi:[1,1,0]
	v_pk_fma_f32 v[164:165], v[120:121], v[146:147], 0 op_sel_hi:[1,1,0]
	v_pk_fma_f32 v[162:163], v[102:103], v[148:149], v[162:163]
	v_pk_fma_f32 v[164:165], v[118:119], v[148:149], v[164:165]
	ds_read_b128 v[146:149], v125 offset:28672
	s_waitcnt lgkmcnt(7)
	v_pk_fma_f32 v[162:163], v[100:101], v[150:151], v[162:163]
	v_pk_fma_f32 v[164:165], v[116:117], v[150:151], v[164:165]
	v_pk_fma_f32 v[162:163], v[98:99], v[152:153], v[162:163]
	v_pk_fma_f32 v[164:165], v[114:115], v[152:153], v[164:165]
	ds_read_b128 v[150:153], v125 offset:29696
	s_waitcnt lgkmcnt(7)
	v_pk_fma_f32 v[162:163], v[96:97], v[154:155], v[162:163]
	v_pk_fma_f32 v[164:165], v[112:113], v[154:155], v[164:165]
	v_pk_fma_f32 v[162:163], v[94:95], v[156:157], v[162:163]
	v_pk_fma_f32 v[164:165], v[110:111], v[156:157], v[164:165]
	ds_read_b128 v[154:157], v125 offset:30720
	s_waitcnt lgkmcnt(7)
	v_pk_fma_f32 v[162:163], v[92:93], v[158:159], v[162:163]
	v_pk_fma_f32 v[164:165], v[108:109], v[158:159], v[164:165]
	v_pk_fma_f32 v[162:163], v[90:91], v[160:161], v[162:163]
	v_pk_fma_f32 v[164:165], v[106:107], v[160:161], v[164:165]
	v_add_f32_e32 v188, v162, v163
	v_add_f32_e32 v183, v164, v165
	ds_read_b128 v[158:161], v125 offset:31744
	s_waitcnt lgkmcnt(7)
	v_pk_fma_f32 v[162:163], v[104:105], v[130:131], 0 op_sel_hi:[1,1,0]
	v_pk_fma_f32 v[164:165], v[120:121], v[130:131], 0 op_sel_hi:[1,1,0]
	v_pk_fma_f32 v[162:163], v[102:103], v[132:133], v[162:163]
	v_pk_fma_f32 v[164:165], v[118:119], v[132:133], v[164:165]
	ds_read_b128 v[130:133], v125 offset:32768
	s_waitcnt lgkmcnt(7)
	v_pk_fma_f32 v[162:163], v[100:101], v[134:135], v[162:163]
	v_pk_fma_f32 v[164:165], v[116:117], v[134:135], v[164:165]
	v_pk_fma_f32 v[162:163], v[98:99], v[136:137], v[162:163]
	v_pk_fma_f32 v[164:165], v[114:115], v[136:137], v[164:165]
	ds_read_b128 v[134:137], v125 offset:33792
	s_waitcnt lgkmcnt(7)
	v_pk_fma_f32 v[162:163], v[96:97], v[138:139], v[162:163]
	v_pk_fma_f32 v[164:165], v[112:113], v[138:139], v[164:165]
	v_pk_fma_f32 v[162:163], v[94:95], v[140:141], v[162:163]
	v_pk_fma_f32 v[164:165], v[110:111], v[140:141], v[164:165]
	ds_read_b128 v[138:141], v125 offset:34816
	s_waitcnt lgkmcnt(7)
	v_pk_fma_f32 v[162:163], v[92:93], v[142:143], v[162:163]
	v_pk_fma_f32 v[164:165], v[108:109], v[142:143], v[164:165]
	v_pk_fma_f32 v[162:163], v[90:91], v[144:145], v[162:163]
	v_pk_fma_f32 v[164:165], v[106:107], v[144:145], v[164:165]
	v_add_f32_e32 v190, v162, v163
	v_add_f32_e32 v185, v164, v165
	ds_read_b128 v[142:145], v125 offset:35840
	s_waitcnt lgkmcnt(7)
	v_pk_fma_f32 v[162:163], v[104:105], v[146:147], 0 op_sel_hi:[1,1,0]
	v_pk_fma_f32 v[164:165], v[120:121], v[146:147], 0 op_sel_hi:[1,1,0]
	v_pk_fma_f32 v[162:163], v[102:103], v[148:149], v[162:163]
	v_pk_fma_f32 v[164:165], v[118:119], v[148:149], v[164:165]
	ds_read_b128 v[146:149], v125 offset:36864
	s_waitcnt lgkmcnt(7)
	v_pk_fma_f32 v[162:163], v[100:101], v[150:151], v[162:163]
	v_pk_fma_f32 v[164:165], v[116:117], v[150:151], v[164:165]
	v_pk_fma_f32 v[162:163], v[98:99], v[152:153], v[162:163]
	v_pk_fma_f32 v[164:165], v[114:115], v[152:153], v[164:165]
	ds_read_b128 v[150:153], v125 offset:37888
	s_waitcnt lgkmcnt(7)
	v_pk_fma_f32 v[162:163], v[96:97], v[154:155], v[162:163]
	v_pk_fma_f32 v[164:165], v[112:113], v[154:155], v[164:165]
	v_pk_fma_f32 v[162:163], v[94:95], v[156:157], v[162:163]
	v_pk_fma_f32 v[164:165], v[110:111], v[156:157], v[164:165]
	ds_read_b128 v[154:157], v125 offset:38912
	s_waitcnt lgkmcnt(7)
	v_pk_fma_f32 v[162:163], v[92:93], v[158:159], v[162:163]
	v_pk_fma_f32 v[164:165], v[108:109], v[158:159], v[164:165]
	v_pk_fma_f32 v[162:163], v[90:91], v[160:161], v[162:163]
	v_pk_fma_f32 v[164:165], v[106:107], v[160:161], v[164:165]
	v_add_f32_e32 v192, v162, v163
	v_add_f32_e32 v187, v164, v165
	ds_read_b128 v[158:161], v125 offset:39936
	s_waitcnt lgkmcnt(7)
	v_pk_fma_f32 v[162:163], v[104:105], v[130:131], 0 op_sel_hi:[1,1,0]
	v_pk_fma_f32 v[164:165], v[120:121], v[130:131], 0 op_sel_hi:[1,1,0]
	v_pk_fma_f32 v[162:163], v[102:103], v[132:133], v[162:163]
	v_pk_fma_f32 v[164:165], v[118:119], v[132:133], v[164:165]
	ds_read_b128 v[130:133], v125 offset:40960
	s_waitcnt lgkmcnt(7)
	v_pk_fma_f32 v[162:163], v[100:101], v[134:135], v[162:163]
	v_pk_fma_f32 v[164:165], v[116:117], v[134:135], v[164:165]
	v_pk_fma_f32 v[162:163], v[98:99], v[136:137], v[162:163]
	v_pk_fma_f32 v[164:165], v[114:115], v[136:137], v[164:165]
	ds_read_b128 v[134:137], v125 offset:41984
	s_waitcnt lgkmcnt(7)
	v_pk_fma_f32 v[162:163], v[96:97], v[138:139], v[162:163]
	v_pk_fma_f32 v[164:165], v[112:113], v[138:139], v[164:165]
	v_pk_fma_f32 v[162:163], v[94:95], v[140:141], v[162:163]
	v_pk_fma_f32 v[164:165], v[110:111], v[140:141], v[164:165]
	ds_read_b128 v[138:141], v125 offset:43008
	s_waitcnt lgkmcnt(7)
	v_pk_fma_f32 v[162:163], v[92:93], v[142:143], v[162:163]
	v_pk_fma_f32 v[164:165], v[108:109], v[142:143], v[164:165]
	v_pk_fma_f32 v[162:163], v[90:91], v[144:145], v[162:163]
	v_pk_fma_f32 v[164:165], v[106:107], v[144:145], v[164:165]
	v_add_f32_e32 v194, v162, v163
	v_add_f32_e32 v189, v164, v165
	ds_read_b128 v[142:145], v125 offset:44032
	s_waitcnt lgkmcnt(7)
	v_pk_fma_f32 v[162:163], v[104:105], v[146:147], 0 op_sel_hi:[1,1,0]
	v_pk_fma_f32 v[164:165], v[120:121], v[146:147], 0 op_sel_hi:[1,1,0]
	v_pk_fma_f32 v[162:163], v[102:103], v[148:149], v[162:163]
	v_pk_fma_f32 v[164:165], v[118:119], v[148:149], v[164:165]
	ds_read_b128 v[146:149], v125 offset:45056
	s_waitcnt lgkmcnt(7)
	v_pk_fma_f32 v[162:163], v[100:101], v[150:151], v[162:163]
	v_pk_fma_f32 v[164:165], v[116:117], v[150:151], v[164:165]
	v_pk_fma_f32 v[162:163], v[98:99], v[152:153], v[162:163]
	v_pk_fma_f32 v[164:165], v[114:115], v[152:153], v[164:165]
	ds_read_b128 v[150:153], v125 offset:46080
	s_waitcnt lgkmcnt(7)
	v_pk_fma_f32 v[162:163], v[96:97], v[154:155], v[162:163]
	v_pk_fma_f32 v[164:165], v[112:113], v[154:155], v[164:165]
	v_pk_fma_f32 v[162:163], v[94:95], v[156:157], v[162:163]
	v_pk_fma_f32 v[164:165], v[110:111], v[156:157], v[164:165]
	ds_read_b128 v[154:157], v125 offset:47104
	s_waitcnt lgkmcnt(7)
	v_pk_fma_f32 v[162:163], v[92:93], v[158:159], v[162:163]
	v_pk_fma_f32 v[164:165], v[108:109], v[158:159], v[164:165]
	v_pk_fma_f32 v[162:163], v[90:91], v[160:161], v[162:163]
	v_pk_fma_f32 v[164:165], v[106:107], v[160:161], v[164:165]
	v_add_f32_e32 v196, v162, v163
	v_add_f32_e32 v191, v164, v165
	ds_read_b128 v[158:161], v125 offset:48128
	s_waitcnt lgkmcnt(7)
	v_pk_fma_f32 v[162:163], v[104:105], v[130:131], 0 op_sel_hi:[1,1,0]
	v_pk_fma_f32 v[164:165], v[120:121], v[130:131], 0 op_sel_hi:[1,1,0]
	v_pk_fma_f32 v[162:163], v[102:103], v[132:133], v[162:163]
	v_pk_fma_f32 v[164:165], v[118:119], v[132:133], v[164:165]
	ds_read_b128 v[130:133], v125 offset:49152
	s_waitcnt lgkmcnt(7)
	v_pk_fma_f32 v[162:163], v[100:101], v[134:135], v[162:163]
	v_pk_fma_f32 v[164:165], v[116:117], v[134:135], v[164:165]
	v_pk_fma_f32 v[162:163], v[98:99], v[136:137], v[162:163]
	v_pk_fma_f32 v[164:165], v[114:115], v[136:137], v[164:165]
	ds_read_b128 v[134:137], v125 offset:50176
	s_waitcnt lgkmcnt(7)
	v_pk_fma_f32 v[162:163], v[96:97], v[138:139], v[162:163]
	v_pk_fma_f32 v[164:165], v[112:113], v[138:139], v[164:165]
	v_pk_fma_f32 v[162:163], v[94:95], v[140:141], v[162:163]
	v_pk_fma_f32 v[164:165], v[110:111], v[140:141], v[164:165]
	ds_read_b128 v[138:141], v125 offset:51200
	s_waitcnt lgkmcnt(7)
	v_pk_fma_f32 v[162:163], v[92:93], v[142:143], v[162:163]
	v_pk_fma_f32 v[164:165], v[108:109], v[142:143], v[164:165]
	v_pk_fma_f32 v[162:163], v[90:91], v[144:145], v[162:163]
	v_pk_fma_f32 v[164:165], v[106:107], v[144:145], v[164:165]
	v_add_f32_e32 v198, v162, v163
	v_add_f32_e32 v193, v164, v165
	ds_read_b128 v[142:145], v125 offset:52224
	s_waitcnt lgkmcnt(7)
	v_pk_fma_f32 v[162:163], v[104:105], v[146:147], 0 op_sel_hi:[1,1,0]
	v_pk_fma_f32 v[164:165], v[120:121], v[146:147], 0 op_sel_hi:[1,1,0]
	v_pk_fma_f32 v[162:163], v[102:103], v[148:149], v[162:163]
	v_pk_fma_f32 v[164:165], v[118:119], v[148:149], v[164:165]
	ds_read_b128 v[146:149], v125 offset:53248
	s_waitcnt lgkmcnt(7)
	v_pk_fma_f32 v[162:163], v[100:101], v[150:151], v[162:163]
	v_pk_fma_f32 v[164:165], v[116:117], v[150:151], v[164:165]
	v_pk_fma_f32 v[162:163], v[98:99], v[152:153], v[162:163]
	v_pk_fma_f32 v[164:165], v[114:115], v[152:153], v[164:165]
	ds_read_b128 v[150:153], v125 offset:54272
	s_waitcnt lgkmcnt(7)
	v_pk_fma_f32 v[162:163], v[96:97], v[154:155], v[162:163]
	v_pk_fma_f32 v[164:165], v[112:113], v[154:155], v[164:165]
	v_pk_fma_f32 v[162:163], v[94:95], v[156:157], v[162:163]
	v_pk_fma_f32 v[164:165], v[110:111], v[156:157], v[164:165]
	ds_read_b128 v[154:157], v125 offset:55296
	s_waitcnt lgkmcnt(7)
	v_pk_fma_f32 v[162:163], v[92:93], v[158:159], v[162:163]
	v_pk_fma_f32 v[164:165], v[108:109], v[158:159], v[164:165]
	v_pk_fma_f32 v[162:163], v[90:91], v[160:161], v[162:163]
	v_pk_fma_f32 v[164:165], v[106:107], v[160:161], v[164:165]
	v_add_f32_e32 v208, v162, v163
	v_add_f32_e32 v195, v164, v165
	ds_read_b128 v[158:161], v125 offset:56320
	s_waitcnt lgkmcnt(7)
	v_pk_fma_f32 v[162:163], v[104:105], v[130:131], 0 op_sel_hi:[1,1,0]
	v_pk_fma_f32 v[164:165], v[120:121], v[130:131], 0 op_sel_hi:[1,1,0]
	v_pk_fma_f32 v[162:163], v[102:103], v[132:133], v[162:163]
	v_pk_fma_f32 v[164:165], v[118:119], v[132:133], v[164:165]
	ds_read_b128 v[130:133], v125 offset:57344
	s_waitcnt lgkmcnt(7)
	v_pk_fma_f32 v[162:163], v[100:101], v[134:135], v[162:163]
	v_pk_fma_f32 v[164:165], v[116:117], v[134:135], v[164:165]
	v_pk_fma_f32 v[162:163], v[98:99], v[136:137], v[162:163]
	v_pk_fma_f32 v[164:165], v[114:115], v[136:137], v[164:165]
	ds_read_b128 v[134:137], v125 offset:58368
	s_waitcnt lgkmcnt(7)
	v_pk_fma_f32 v[162:163], v[96:97], v[138:139], v[162:163]
	v_pk_fma_f32 v[164:165], v[112:113], v[138:139], v[164:165]
	v_pk_fma_f32 v[162:163], v[94:95], v[140:141], v[162:163]
	v_pk_fma_f32 v[164:165], v[110:111], v[140:141], v[164:165]
	ds_read_b128 v[138:141], v125 offset:59392
	s_waitcnt lgkmcnt(7)
	v_pk_fma_f32 v[162:163], v[92:93], v[142:143], v[162:163]
	v_pk_fma_f32 v[164:165], v[108:109], v[142:143], v[164:165]
	v_pk_fma_f32 v[162:163], v[90:91], v[144:145], v[162:163]
	v_pk_fma_f32 v[164:165], v[106:107], v[144:145], v[164:165]
	v_add_f32_e32 v213, v162, v163
	v_add_f32_e32 v197, v164, v165
	ds_read_b128 v[142:145], v125 offset:60416
	s_waitcnt lgkmcnt(7)
	v_pk_fma_f32 v[162:163], v[104:105], v[146:147], 0 op_sel_hi:[1,1,0]
	v_pk_fma_f32 v[164:165], v[120:121], v[146:147], 0 op_sel_hi:[1,1,0]
	v_pk_fma_f32 v[162:163], v[102:103], v[148:149], v[162:163]
	v_pk_fma_f32 v[164:165], v[118:119], v[148:149], v[164:165]
	ds_read_b128 v[146:149], v125 offset:61440
	s_waitcnt lgkmcnt(7)
	v_pk_fma_f32 v[162:163], v[100:101], v[150:151], v[162:163]
	v_pk_fma_f32 v[164:165], v[116:117], v[150:151], v[164:165]
	v_pk_fma_f32 v[162:163], v[98:99], v[152:153], v[162:163]
	v_pk_fma_f32 v[164:165], v[114:115], v[152:153], v[164:165]
	ds_read_b128 v[150:153], v125 offset:62464
	s_waitcnt lgkmcnt(7)
	v_pk_fma_f32 v[162:163], v[96:97], v[154:155], v[162:163]
	v_pk_fma_f32 v[164:165], v[112:113], v[154:155], v[164:165]
	v_pk_fma_f32 v[162:163], v[94:95], v[156:157], v[162:163]
	v_pk_fma_f32 v[164:165], v[110:111], v[156:157], v[164:165]
	ds_read_b128 v[154:157], v125 offset:63488
	s_waitcnt lgkmcnt(7)
	v_pk_fma_f32 v[162:163], v[92:93], v[158:159], v[162:163]
	v_pk_fma_f32 v[164:165], v[108:109], v[158:159], v[164:165]
	v_pk_fma_f32 v[162:163], v[90:91], v[160:161], v[162:163]
	v_pk_fma_f32 v[164:165], v[106:107], v[160:161], v[164:165]
	v_add_f32_e32 v215, v162, v163
	v_add_f32_e32 v199, v164, v165
	ds_read_b128 v[158:161], v125 offset:64512
	s_waitcnt lgkmcnt(7)
	v_pk_fma_f32 v[162:163], v[104:105], v[130:131], 0 op_sel_hi:[1,1,0]
	v_pk_fma_f32 v[164:165], v[120:121], v[130:131], 0 op_sel_hi:[1,1,0]
	v_pk_fma_f32 v[162:163], v[102:103], v[132:133], v[162:163]
	v_pk_fma_f32 v[164:165], v[118:119], v[132:133], v[164:165]
	ds_read_b128 v[130:133], v129
	s_waitcnt lgkmcnt(7)
	v_pk_fma_f32 v[162:163], v[100:101], v[134:135], v[162:163]
	v_pk_fma_f32 v[164:165], v[116:117], v[134:135], v[164:165]
	v_pk_fma_f32 v[162:163], v[98:99], v[136:137], v[162:163]
	v_pk_fma_f32 v[164:165], v[114:115], v[136:137], v[164:165]
	ds_read_b128 v[134:137], v129 offset:1024
	s_waitcnt lgkmcnt(7)
	v_pk_fma_f32 v[162:163], v[96:97], v[138:139], v[162:163]
	v_pk_fma_f32 v[164:165], v[112:113], v[138:139], v[164:165]
	v_pk_fma_f32 v[162:163], v[94:95], v[140:141], v[162:163]
	v_pk_fma_f32 v[164:165], v[110:111], v[140:141], v[164:165]
	ds_read_b128 v[138:141], v129 offset:2048
	s_waitcnt lgkmcnt(7)
	v_pk_fma_f32 v[162:163], v[92:93], v[142:143], v[162:163]
	v_pk_fma_f32 v[164:165], v[108:109], v[142:143], v[164:165]
	v_pk_fma_f32 v[162:163], v[90:91], v[144:145], v[162:163]
	v_pk_fma_f32 v[164:165], v[106:107], v[144:145], v[164:165]
	v_add_f32_e32 v216, v162, v163
	v_add_f32_e32 v209, v164, v165
	ds_read_b128 v[142:145], v129 offset:3072
	s_waitcnt lgkmcnt(7)
	v_pk_fma_f32 v[162:163], v[104:105], v[146:147], 0 op_sel_hi:[1,1,0]
	v_pk_fma_f32 v[164:165], v[120:121], v[146:147], 0 op_sel_hi:[1,1,0]
	v_pk_fma_f32 v[162:163], v[102:103], v[148:149], v[162:163]
	v_pk_fma_f32 v[164:165], v[118:119], v[148:149], v[164:165]
	ds_read_b128 v[146:149], v129 offset:4096
	s_waitcnt lgkmcnt(7)
	v_pk_fma_f32 v[162:163], v[100:101], v[150:151], v[162:163]
	v_pk_fma_f32 v[164:165], v[116:117], v[150:151], v[164:165]
	v_pk_fma_f32 v[162:163], v[98:99], v[152:153], v[162:163]
	v_pk_fma_f32 v[164:165], v[114:115], v[152:153], v[164:165]
	ds_read_b128 v[150:153], v129 offset:5120
	s_waitcnt lgkmcnt(7)
	v_pk_fma_f32 v[162:163], v[96:97], v[154:155], v[162:163]
	v_pk_fma_f32 v[164:165], v[112:113], v[154:155], v[164:165]
	v_pk_fma_f32 v[162:163], v[94:95], v[156:157], v[162:163]
	v_pk_fma_f32 v[164:165], v[110:111], v[156:157], v[164:165]
	ds_read_b128 v[154:157], v129 offset:6144
	s_waitcnt lgkmcnt(7)
	v_pk_fma_f32 v[162:163], v[92:93], v[158:159], v[162:163]
	v_pk_fma_f32 v[164:165], v[108:109], v[158:159], v[164:165]
	v_pk_fma_f32 v[162:163], v[90:91], v[160:161], v[162:163]
	v_pk_fma_f32 v[164:165], v[106:107], v[160:161], v[164:165]
	v_add_f32_e32 v218, v162, v163
	v_add_f32_e32 v214, v164, v165
	ds_read_b128 v[158:161], v129 offset:7168
	s_waitcnt lgkmcnt(7)
	v_pk_fma_f32 v[162:163], v[104:105], v[130:131], 0 op_sel_hi:[1,1,0]
	v_pk_fma_f32 v[164:165], v[120:121], v[130:131], 0 op_sel_hi:[1,1,0]
	v_pk_fma_f32 v[162:163], v[102:103], v[132:133], v[162:163]
	v_pk_fma_f32 v[164:165], v[118:119], v[132:133], v[164:165]
	ds_read_b128 v[130:133], v129 offset:8192
	s_waitcnt lgkmcnt(7)
	v_pk_fma_f32 v[162:163], v[100:101], v[134:135], v[162:163]
	v_pk_fma_f32 v[164:165], v[116:117], v[134:135], v[164:165]
	v_pk_fma_f32 v[162:163], v[98:99], v[136:137], v[162:163]
	v_pk_fma_f32 v[164:165], v[114:115], v[136:137], v[164:165]
	ds_read_b128 v[134:137], v129 offset:9216
	s_waitcnt lgkmcnt(7)
	v_pk_fma_f32 v[162:163], v[96:97], v[138:139], v[162:163]
	v_pk_fma_f32 v[164:165], v[112:113], v[138:139], v[164:165]
	v_pk_fma_f32 v[162:163], v[94:95], v[140:141], v[162:163]
	v_pk_fma_f32 v[164:165], v[110:111], v[140:141], v[164:165]
	ds_read_b128 v[138:141], v129 offset:10240
	s_waitcnt lgkmcnt(7)
	v_pk_fma_f32 v[162:163], v[92:93], v[142:143], v[162:163]
	v_pk_fma_f32 v[164:165], v[108:109], v[142:143], v[164:165]
	v_pk_fma_f32 v[162:163], v[90:91], v[144:145], v[162:163]
	v_pk_fma_f32 v[164:165], v[106:107], v[144:145], v[164:165]
	v_add_f32_e32 v221, v162, v163
	v_add_f32_e32 v217, v164, v165
	ds_read_b128 v[142:145], v129 offset:11264
	s_waitcnt lgkmcnt(7)
	v_pk_fma_f32 v[162:163], v[104:105], v[146:147], 0 op_sel_hi:[1,1,0]
	v_pk_fma_f32 v[164:165], v[120:121], v[146:147], 0 op_sel_hi:[1,1,0]
	v_pk_fma_f32 v[162:163], v[102:103], v[148:149], v[162:163]
	v_pk_fma_f32 v[164:165], v[118:119], v[148:149], v[164:165]
	ds_read_b128 v[146:149], v129 offset:12288
	s_waitcnt lgkmcnt(7)
	v_pk_fma_f32 v[162:163], v[100:101], v[150:151], v[162:163]
	v_pk_fma_f32 v[164:165], v[116:117], v[150:151], v[164:165]
	v_pk_fma_f32 v[162:163], v[98:99], v[152:153], v[162:163]
	v_pk_fma_f32 v[164:165], v[114:115], v[152:153], v[164:165]
	ds_read_b128 v[150:153], v129 offset:13312
	s_waitcnt lgkmcnt(7)
	v_pk_fma_f32 v[162:163], v[96:97], v[154:155], v[162:163]
	v_pk_fma_f32 v[164:165], v[112:113], v[154:155], v[164:165]
	v_pk_fma_f32 v[162:163], v[94:95], v[156:157], v[162:163]
	v_pk_fma_f32 v[164:165], v[110:111], v[156:157], v[164:165]
	ds_read_b128 v[154:157], v129 offset:14336
	s_waitcnt lgkmcnt(7)
	v_pk_fma_f32 v[162:163], v[92:93], v[158:159], v[162:163]
	v_pk_fma_f32 v[164:165], v[108:109], v[158:159], v[164:165]
	v_pk_fma_f32 v[162:163], v[90:91], v[160:161], v[162:163]
	v_pk_fma_f32 v[164:165], v[106:107], v[160:161], v[164:165]
	v_add_f32_e32 v223, v162, v163
	v_add_f32_e32 v219, v164, v165
	ds_read_b128 v[158:161], v129 offset:15360
	s_waitcnt lgkmcnt(7)
	v_pk_fma_f32 v[162:163], v[104:105], v[130:131], 0 op_sel_hi:[1,1,0]
	v_pk_fma_f32 v[164:165], v[120:121], v[130:131], 0 op_sel_hi:[1,1,0]
	v_pk_fma_f32 v[162:163], v[102:103], v[132:133], v[162:163]
	v_pk_fma_f32 v[164:165], v[118:119], v[132:133], v[164:165]
	ds_read_b128 v[130:133], v129 offset:16384
	s_waitcnt lgkmcnt(7)
	v_pk_fma_f32 v[162:163], v[100:101], v[134:135], v[162:163]
	v_pk_fma_f32 v[164:165], v[116:117], v[134:135], v[164:165]
	v_pk_fma_f32 v[162:163], v[98:99], v[136:137], v[162:163]
	v_pk_fma_f32 v[164:165], v[114:115], v[136:137], v[164:165]
	ds_read_b128 v[134:137], v129 offset:17408
	s_waitcnt lgkmcnt(7)
	v_pk_fma_f32 v[162:163], v[96:97], v[138:139], v[162:163]
	v_pk_fma_f32 v[164:165], v[112:113], v[138:139], v[164:165]
	v_pk_fma_f32 v[162:163], v[94:95], v[140:141], v[162:163]
	v_pk_fma_f32 v[164:165], v[110:111], v[140:141], v[164:165]
	ds_read_b128 v[138:141], v129 offset:18432
	s_waitcnt lgkmcnt(7)
	v_pk_fma_f32 v[162:163], v[92:93], v[142:143], v[162:163]
	v_pk_fma_f32 v[164:165], v[108:109], v[142:143], v[164:165]
	v_pk_fma_f32 v[162:163], v[90:91], v[144:145], v[162:163]
	v_pk_fma_f32 v[164:165], v[106:107], v[144:145], v[164:165]
	v_add_f32_e32 v225, v162, v163
	v_add_f32_e32 v220, v164, v165
	ds_read_b128 v[142:145], v129 offset:19456
	s_waitcnt lgkmcnt(7)
	v_pk_fma_f32 v[162:163], v[104:105], v[146:147], 0 op_sel_hi:[1,1,0]
	v_pk_fma_f32 v[164:165], v[120:121], v[146:147], 0 op_sel_hi:[1,1,0]
	v_pk_fma_f32 v[162:163], v[102:103], v[148:149], v[162:163]
	v_pk_fma_f32 v[164:165], v[118:119], v[148:149], v[164:165]
	ds_read_b128 v[146:149], v129 offset:20480
	s_waitcnt lgkmcnt(7)
	v_pk_fma_f32 v[162:163], v[100:101], v[150:151], v[162:163]
	v_pk_fma_f32 v[164:165], v[116:117], v[150:151], v[164:165]
	v_pk_fma_f32 v[162:163], v[98:99], v[152:153], v[162:163]
	v_pk_fma_f32 v[164:165], v[114:115], v[152:153], v[164:165]
	ds_read_b128 v[150:153], v129 offset:21504
	s_waitcnt lgkmcnt(7)
	v_pk_fma_f32 v[162:163], v[96:97], v[154:155], v[162:163]
	v_pk_fma_f32 v[164:165], v[112:113], v[154:155], v[164:165]
	v_pk_fma_f32 v[162:163], v[94:95], v[156:157], v[162:163]
	v_pk_fma_f32 v[164:165], v[110:111], v[156:157], v[164:165]
	ds_read_b128 v[154:157], v129 offset:22528
	s_waitcnt lgkmcnt(7)
	v_pk_fma_f32 v[162:163], v[92:93], v[158:159], v[162:163]
	v_pk_fma_f32 v[164:165], v[108:109], v[158:159], v[164:165]
	v_pk_fma_f32 v[162:163], v[90:91], v[160:161], v[162:163]
	v_pk_fma_f32 v[164:165], v[106:107], v[160:161], v[164:165]
	v_add_f32_e32 v227, v162, v163
	v_add_f32_e32 v222, v164, v165
	ds_read_b128 v[158:161], v129 offset:23552
	s_waitcnt lgkmcnt(7)
	v_pk_fma_f32 v[162:163], v[104:105], v[130:131], 0 op_sel_hi:[1,1,0]
	v_pk_fma_f32 v[164:165], v[120:121], v[130:131], 0 op_sel_hi:[1,1,0]
	v_pk_fma_f32 v[162:163], v[102:103], v[132:133], v[162:163]
	v_pk_fma_f32 v[164:165], v[118:119], v[132:133], v[164:165]
	ds_read_b128 v[130:133], v129 offset:24576
	s_waitcnt lgkmcnt(7)
	v_pk_fma_f32 v[162:163], v[100:101], v[134:135], v[162:163]
	v_pk_fma_f32 v[164:165], v[116:117], v[134:135], v[164:165]
	v_pk_fma_f32 v[162:163], v[98:99], v[136:137], v[162:163]
	v_pk_fma_f32 v[164:165], v[114:115], v[136:137], v[164:165]
	ds_read_b128 v[134:137], v129 offset:25600
	s_waitcnt lgkmcnt(7)
	v_pk_fma_f32 v[162:163], v[96:97], v[138:139], v[162:163]
	v_pk_fma_f32 v[164:165], v[112:113], v[138:139], v[164:165]
	v_pk_fma_f32 v[162:163], v[94:95], v[140:141], v[162:163]
	v_pk_fma_f32 v[164:165], v[110:111], v[140:141], v[164:165]
	ds_read_b128 v[138:141], v129 offset:26624
	s_waitcnt lgkmcnt(7)
	v_pk_fma_f32 v[162:163], v[92:93], v[142:143], v[162:163]
	v_pk_fma_f32 v[164:165], v[108:109], v[142:143], v[164:165]
	v_pk_fma_f32 v[162:163], v[90:91], v[144:145], v[162:163]
	v_pk_fma_f32 v[164:165], v[106:107], v[144:145], v[164:165]
	v_add_f32_e32 v229, v162, v163
	v_add_f32_e32 v224, v164, v165
	ds_read_b128 v[142:145], v129 offset:27648
	s_waitcnt lgkmcnt(7)
	v_pk_fma_f32 v[162:163], v[104:105], v[146:147], 0 op_sel_hi:[1,1,0]
	v_pk_fma_f32 v[164:165], v[120:121], v[146:147], 0 op_sel_hi:[1,1,0]
	v_pk_fma_f32 v[162:163], v[102:103], v[148:149], v[162:163]
	v_pk_fma_f32 v[164:165], v[118:119], v[148:149], v[164:165]
	ds_read_b128 v[146:149], v129 offset:28672
	s_waitcnt lgkmcnt(7)
	v_pk_fma_f32 v[162:163], v[100:101], v[150:151], v[162:163]
	v_pk_fma_f32 v[164:165], v[116:117], v[150:151], v[164:165]
	v_pk_fma_f32 v[162:163], v[98:99], v[152:153], v[162:163]
	v_pk_fma_f32 v[164:165], v[114:115], v[152:153], v[164:165]
	ds_read_b128 v[150:153], v129 offset:29696
	s_waitcnt lgkmcnt(7)
	v_pk_fma_f32 v[162:163], v[96:97], v[154:155], v[162:163]
	v_pk_fma_f32 v[164:165], v[112:113], v[154:155], v[164:165]
	v_pk_fma_f32 v[162:163], v[94:95], v[156:157], v[162:163]
	v_pk_fma_f32 v[164:165], v[110:111], v[156:157], v[164:165]
	ds_read_b128 v[154:157], v129 offset:30720
	s_waitcnt lgkmcnt(7)
	v_pk_fma_f32 v[162:163], v[92:93], v[158:159], v[162:163]
	v_pk_fma_f32 v[164:165], v[108:109], v[158:159], v[164:165]
	v_pk_fma_f32 v[162:163], v[90:91], v[160:161], v[162:163]
	v_pk_fma_f32 v[164:165], v[106:107], v[160:161], v[164:165]
	v_add_f32_e32 v231, v162, v163
	v_add_f32_e32 v226, v164, v165
	ds_read_b128 v[158:161], v129 offset:31744
	s_waitcnt lgkmcnt(7)
	v_pk_fma_f32 v[162:163], v[104:105], v[130:131], 0 op_sel_hi:[1,1,0]
	v_pk_fma_f32 v[164:165], v[120:121], v[130:131], 0 op_sel_hi:[1,1,0]
	v_pk_fma_f32 v[162:163], v[102:103], v[132:133], v[162:163]
	v_pk_fma_f32 v[164:165], v[118:119], v[132:133], v[164:165]
	ds_read_b128 v[130:133], v129 offset:32768
	s_waitcnt lgkmcnt(7)
	v_pk_fma_f32 v[162:163], v[100:101], v[134:135], v[162:163]
	v_pk_fma_f32 v[164:165], v[116:117], v[134:135], v[164:165]
	v_pk_fma_f32 v[162:163], v[98:99], v[136:137], v[162:163]
	v_pk_fma_f32 v[164:165], v[114:115], v[136:137], v[164:165]
	ds_read_b128 v[134:137], v129 offset:33792
	s_waitcnt lgkmcnt(7)
	v_pk_fma_f32 v[162:163], v[96:97], v[138:139], v[162:163]
	v_pk_fma_f32 v[164:165], v[112:113], v[138:139], v[164:165]
	v_pk_fma_f32 v[162:163], v[94:95], v[140:141], v[162:163]
	v_pk_fma_f32 v[164:165], v[110:111], v[140:141], v[164:165]
	ds_read_b128 v[138:141], v129 offset:34816
	s_waitcnt lgkmcnt(7)
	v_pk_fma_f32 v[162:163], v[92:93], v[142:143], v[162:163]
	v_pk_fma_f32 v[164:165], v[108:109], v[142:143], v[164:165]
	v_pk_fma_f32 v[162:163], v[90:91], v[144:145], v[162:163]
	v_pk_fma_f32 v[164:165], v[106:107], v[144:145], v[164:165]
	v_add_f32_e32 v233, v162, v163
	v_add_f32_e32 v228, v164, v165
	ds_read_b128 v[142:145], v129 offset:35840
	s_waitcnt lgkmcnt(7)
	v_pk_fma_f32 v[162:163], v[104:105], v[146:147], 0 op_sel_hi:[1,1,0]
	v_pk_fma_f32 v[164:165], v[120:121], v[146:147], 0 op_sel_hi:[1,1,0]
	v_pk_fma_f32 v[162:163], v[102:103], v[148:149], v[162:163]
	v_pk_fma_f32 v[164:165], v[118:119], v[148:149], v[164:165]
	ds_read_b128 v[146:149], v129 offset:36864
	s_waitcnt lgkmcnt(7)
	v_pk_fma_f32 v[162:163], v[100:101], v[150:151], v[162:163]
	v_pk_fma_f32 v[164:165], v[116:117], v[150:151], v[164:165]
	v_pk_fma_f32 v[162:163], v[98:99], v[152:153], v[162:163]
	v_pk_fma_f32 v[164:165], v[114:115], v[152:153], v[164:165]
	ds_read_b128 v[150:153], v129 offset:37888
	s_waitcnt lgkmcnt(7)
	v_pk_fma_f32 v[162:163], v[96:97], v[154:155], v[162:163]
	v_pk_fma_f32 v[164:165], v[112:113], v[154:155], v[164:165]
	v_pk_fma_f32 v[162:163], v[94:95], v[156:157], v[162:163]
	v_pk_fma_f32 v[164:165], v[110:111], v[156:157], v[164:165]
	ds_read_b128 v[154:157], v129 offset:38912
	s_waitcnt lgkmcnt(7)
	v_pk_fma_f32 v[162:163], v[92:93], v[158:159], v[162:163]
	v_pk_fma_f32 v[164:165], v[108:109], v[158:159], v[164:165]
	v_pk_fma_f32 v[162:163], v[90:91], v[160:161], v[162:163]
	v_pk_fma_f32 v[164:165], v[106:107], v[160:161], v[164:165]
	v_add_f32_e32 v235, v162, v163
	v_add_f32_e32 v230, v164, v165
	ds_read_b128 v[158:161], v129 offset:39936
	s_waitcnt lgkmcnt(7)
	v_pk_fma_f32 v[162:163], v[104:105], v[130:131], 0 op_sel_hi:[1,1,0]
	v_pk_fma_f32 v[164:165], v[120:121], v[130:131], 0 op_sel_hi:[1,1,0]
	v_pk_fma_f32 v[162:163], v[102:103], v[132:133], v[162:163]
	v_pk_fma_f32 v[164:165], v[118:119], v[132:133], v[164:165]
	ds_read_b128 v[130:133], v129 offset:40960
	s_waitcnt lgkmcnt(7)
	v_pk_fma_f32 v[162:163], v[100:101], v[134:135], v[162:163]
	v_pk_fma_f32 v[164:165], v[116:117], v[134:135], v[164:165]
	v_pk_fma_f32 v[162:163], v[98:99], v[136:137], v[162:163]
	v_pk_fma_f32 v[164:165], v[114:115], v[136:137], v[164:165]
	ds_read_b128 v[134:137], v129 offset:41984
	s_waitcnt lgkmcnt(7)
	v_pk_fma_f32 v[162:163], v[96:97], v[138:139], v[162:163]
	v_pk_fma_f32 v[164:165], v[112:113], v[138:139], v[164:165]
	v_pk_fma_f32 v[162:163], v[94:95], v[140:141], v[162:163]
	v_pk_fma_f32 v[164:165], v[110:111], v[140:141], v[164:165]
	ds_read_b128 v[138:141], v129 offset:43008
	s_waitcnt lgkmcnt(7)
	v_pk_fma_f32 v[162:163], v[92:93], v[142:143], v[162:163]
	v_pk_fma_f32 v[164:165], v[108:109], v[142:143], v[164:165]
	v_pk_fma_f32 v[162:163], v[90:91], v[144:145], v[162:163]
	v_pk_fma_f32 v[164:165], v[106:107], v[144:145], v[164:165]
	v_add_f32_e32 v237, v162, v163
	v_add_f32_e32 v232, v164, v165
	ds_read_b128 v[142:145], v129 offset:44032
	s_waitcnt lgkmcnt(7)
	v_pk_fma_f32 v[162:163], v[104:105], v[146:147], 0 op_sel_hi:[1,1,0]
	v_pk_fma_f32 v[164:165], v[120:121], v[146:147], 0 op_sel_hi:[1,1,0]
	v_pk_fma_f32 v[162:163], v[102:103], v[148:149], v[162:163]
	v_pk_fma_f32 v[164:165], v[118:119], v[148:149], v[164:165]
	ds_read_b128 v[146:149], v129 offset:45056
	s_waitcnt lgkmcnt(7)
	v_pk_fma_f32 v[162:163], v[100:101], v[150:151], v[162:163]
	v_pk_fma_f32 v[164:165], v[116:117], v[150:151], v[164:165]
	v_pk_fma_f32 v[162:163], v[98:99], v[152:153], v[162:163]
	v_pk_fma_f32 v[164:165], v[114:115], v[152:153], v[164:165]
	ds_read_b128 v[150:153], v129 offset:46080
	s_waitcnt lgkmcnt(7)
	v_pk_fma_f32 v[162:163], v[96:97], v[154:155], v[162:163]
	v_pk_fma_f32 v[164:165], v[112:113], v[154:155], v[164:165]
	v_pk_fma_f32 v[162:163], v[94:95], v[156:157], v[162:163]
	v_pk_fma_f32 v[164:165], v[110:111], v[156:157], v[164:165]
	ds_read_b128 v[154:157], v129 offset:47104
	s_waitcnt lgkmcnt(7)
	v_pk_fma_f32 v[162:163], v[92:93], v[158:159], v[162:163]
	v_pk_fma_f32 v[164:165], v[108:109], v[158:159], v[164:165]
	v_pk_fma_f32 v[162:163], v[90:91], v[160:161], v[162:163]
	v_pk_fma_f32 v[164:165], v[106:107], v[160:161], v[164:165]
	v_add_f32_e32 v239, v162, v163
	v_add_f32_e32 v234, v164, v165
	ds_read_b128 v[158:161], v129 offset:48128
	s_waitcnt lgkmcnt(7)
	v_pk_fma_f32 v[162:163], v[104:105], v[130:131], 0 op_sel_hi:[1,1,0]
	v_pk_fma_f32 v[164:165], v[120:121], v[130:131], 0 op_sel_hi:[1,1,0]
	v_pk_fma_f32 v[162:163], v[102:103], v[132:133], v[162:163]
	v_pk_fma_f32 v[164:165], v[118:119], v[132:133], v[164:165]
	ds_read_b128 v[130:133], v129 offset:49152
	s_waitcnt lgkmcnt(7)
	v_pk_fma_f32 v[162:163], v[100:101], v[134:135], v[162:163]
	v_pk_fma_f32 v[164:165], v[116:117], v[134:135], v[164:165]
	v_pk_fma_f32 v[162:163], v[98:99], v[136:137], v[162:163]
	v_pk_fma_f32 v[164:165], v[114:115], v[136:137], v[164:165]
	ds_read_b128 v[134:137], v129 offset:50176
	s_waitcnt lgkmcnt(7)
	v_pk_fma_f32 v[162:163], v[96:97], v[138:139], v[162:163]
	v_pk_fma_f32 v[164:165], v[112:113], v[138:139], v[164:165]
	v_pk_fma_f32 v[162:163], v[94:95], v[140:141], v[162:163]
	v_pk_fma_f32 v[164:165], v[110:111], v[140:141], v[164:165]
	ds_read_b128 v[138:141], v129 offset:51200
	s_waitcnt lgkmcnt(7)
	v_pk_fma_f32 v[162:163], v[92:93], v[142:143], v[162:163]
	v_pk_fma_f32 v[164:165], v[108:109], v[142:143], v[164:165]
	v_pk_fma_f32 v[162:163], v[90:91], v[144:145], v[162:163]
	v_pk_fma_f32 v[164:165], v[106:107], v[144:145], v[164:165]
	v_add_f32_e32 v241, v162, v163
	v_add_f32_e32 v236, v164, v165
	ds_read_b128 v[142:145], v129 offset:52224
	s_waitcnt lgkmcnt(7)
	v_pk_fma_f32 v[162:163], v[104:105], v[146:147], 0 op_sel_hi:[1,1,0]
	v_pk_fma_f32 v[164:165], v[120:121], v[146:147], 0 op_sel_hi:[1,1,0]
	v_pk_fma_f32 v[162:163], v[102:103], v[148:149], v[162:163]
	v_pk_fma_f32 v[164:165], v[118:119], v[148:149], v[164:165]
	ds_read_b128 v[146:149], v129 offset:53248
	s_waitcnt lgkmcnt(7)
	v_pk_fma_f32 v[162:163], v[100:101], v[150:151], v[162:163]
	v_pk_fma_f32 v[164:165], v[116:117], v[150:151], v[164:165]
	v_pk_fma_f32 v[162:163], v[98:99], v[152:153], v[162:163]
	v_pk_fma_f32 v[164:165], v[114:115], v[152:153], v[164:165]
	ds_read_b128 v[150:153], v129 offset:54272
	s_waitcnt lgkmcnt(7)
	v_pk_fma_f32 v[162:163], v[96:97], v[154:155], v[162:163]
	v_pk_fma_f32 v[164:165], v[112:113], v[154:155], v[164:165]
	v_pk_fma_f32 v[162:163], v[94:95], v[156:157], v[162:163]
	v_pk_fma_f32 v[164:165], v[110:111], v[156:157], v[164:165]
	ds_read_b128 v[154:157], v129 offset:55296
	s_waitcnt lgkmcnt(7)
	v_pk_fma_f32 v[162:163], v[92:93], v[158:159], v[162:163]
	v_pk_fma_f32 v[164:165], v[108:109], v[158:159], v[164:165]
	v_pk_fma_f32 v[162:163], v[90:91], v[160:161], v[162:163]
	v_pk_fma_f32 v[164:165], v[106:107], v[160:161], v[164:165]
	v_add_f32_e32 v243, v162, v163
	v_add_f32_e32 v238, v164, v165
	ds_read_b128 v[158:161], v129 offset:56320
	s_waitcnt lgkmcnt(7)
	v_pk_fma_f32 v[162:163], v[104:105], v[130:131], 0 op_sel_hi:[1,1,0]
	v_pk_fma_f32 v[164:165], v[120:121], v[130:131], 0 op_sel_hi:[1,1,0]
	v_pk_fma_f32 v[162:163], v[102:103], v[132:133], v[162:163]
	v_pk_fma_f32 v[164:165], v[118:119], v[132:133], v[164:165]
	ds_read_b128 v[130:133], v129 offset:57344
	s_waitcnt lgkmcnt(7)
	v_pk_fma_f32 v[162:163], v[100:101], v[134:135], v[162:163]
	v_pk_fma_f32 v[164:165], v[116:117], v[134:135], v[164:165]
	v_pk_fma_f32 v[162:163], v[98:99], v[136:137], v[162:163]
	v_pk_fma_f32 v[164:165], v[114:115], v[136:137], v[164:165]
	ds_read_b128 v[134:137], v129 offset:58368
	s_waitcnt lgkmcnt(7)
	v_pk_fma_f32 v[162:163], v[96:97], v[138:139], v[162:163]
	v_pk_fma_f32 v[164:165], v[112:113], v[138:139], v[164:165]
	v_pk_fma_f32 v[162:163], v[94:95], v[140:141], v[162:163]
	v_pk_fma_f32 v[164:165], v[110:111], v[140:141], v[164:165]
	ds_read_b128 v[138:141], v129 offset:59392
	s_waitcnt lgkmcnt(7)
	v_pk_fma_f32 v[162:163], v[92:93], v[142:143], v[162:163]
	v_pk_fma_f32 v[164:165], v[108:109], v[142:143], v[164:165]
	v_pk_fma_f32 v[162:163], v[90:91], v[144:145], v[162:163]
	v_pk_fma_f32 v[164:165], v[106:107], v[144:145], v[164:165]
	v_add_f32_e32 v245, v162, v163
	v_add_f32_e32 v240, v164, v165
	ds_read_b128 v[142:145], v129 offset:60416
	s_waitcnt lgkmcnt(7)
	v_pk_fma_f32 v[162:163], v[104:105], v[146:147], 0 op_sel_hi:[1,1,0]
	v_pk_fma_f32 v[164:165], v[120:121], v[146:147], 0 op_sel_hi:[1,1,0]
	v_pk_fma_f32 v[162:163], v[102:103], v[148:149], v[162:163]
	v_pk_fma_f32 v[164:165], v[118:119], v[148:149], v[164:165]
	ds_read_b128 v[146:149], v129 offset:61440
	s_waitcnt lgkmcnt(7)
	v_pk_fma_f32 v[162:163], v[100:101], v[150:151], v[162:163]
	v_pk_fma_f32 v[164:165], v[116:117], v[150:151], v[164:165]
	v_pk_fma_f32 v[162:163], v[98:99], v[152:153], v[162:163]
	v_pk_fma_f32 v[164:165], v[114:115], v[152:153], v[164:165]
	ds_read_b128 v[150:153], v129 offset:62464
	s_waitcnt lgkmcnt(7)
	v_pk_fma_f32 v[162:163], v[96:97], v[154:155], v[162:163]
	v_pk_fma_f32 v[164:165], v[112:113], v[154:155], v[164:165]
	v_pk_fma_f32 v[162:163], v[94:95], v[156:157], v[162:163]
	v_pk_fma_f32 v[164:165], v[110:111], v[156:157], v[164:165]
	ds_read_b128 v[154:157], v129 offset:63488
	s_waitcnt lgkmcnt(7)
	v_pk_fma_f32 v[162:163], v[92:93], v[158:159], v[162:163]
	v_pk_fma_f32 v[164:165], v[108:109], v[158:159], v[164:165]
	v_pk_fma_f32 v[162:163], v[90:91], v[160:161], v[162:163]
	v_pk_fma_f32 v[164:165], v[106:107], v[160:161], v[164:165]
	v_add_f32_e32 v212, v162, v163
	v_add_f32_e32 v242, v164, v165
	ds_read_b128 v[158:161], v129 offset:64512
	s_waitcnt lgkmcnt(7)
	v_pk_fma_f32 v[162:163], v[104:105], v[130:131], 0 op_sel_hi:[1,1,0]
	v_pk_fma_f32 v[164:165], v[120:121], v[130:131], 0 op_sel_hi:[1,1,0]
	v_pk_fma_f32 v[162:163], v[102:103], v[132:133], v[162:163]
	v_pk_fma_f32 v[164:165], v[118:119], v[132:133], v[164:165]
	s_waitcnt lgkmcnt(6)
	v_pk_fma_f32 v[162:163], v[100:101], v[134:135], v[162:163]
	v_pk_fma_f32 v[164:165], v[116:117], v[134:135], v[164:165]
	v_pk_fma_f32 v[162:163], v[98:99], v[136:137], v[162:163]
	v_pk_fma_f32 v[164:165], v[114:115], v[136:137], v[164:165]
	s_waitcnt lgkmcnt(5)
	v_pk_fma_f32 v[162:163], v[96:97], v[138:139], v[162:163]
	v_pk_fma_f32 v[164:165], v[112:113], v[138:139], v[164:165]
	v_pk_fma_f32 v[162:163], v[94:95], v[140:141], v[162:163]
	v_pk_fma_f32 v[164:165], v[110:111], v[140:141], v[164:165]
	s_waitcnt lgkmcnt(4)
	v_pk_fma_f32 v[162:163], v[92:93], v[142:143], v[162:163]
	v_pk_fma_f32 v[164:165], v[108:109], v[142:143], v[164:165]
	v_pk_fma_f32 v[162:163], v[90:91], v[144:145], v[162:163]
	v_pk_fma_f32 v[164:165], v[106:107], v[144:145], v[164:165]
	v_add_f32_e32 v210, v162, v163
	v_add_f32_e32 v244, v164, v165
	s_waitcnt lgkmcnt(3)
	v_pk_fma_f32 v[162:163], v[104:105], v[146:147], 0 op_sel_hi:[1,1,0]
	v_pk_fma_f32 v[164:165], v[120:121], v[146:147], 0 op_sel_hi:[1,1,0]
	v_pk_fma_f32 v[162:163], v[102:103], v[148:149], v[162:163]
	v_pk_fma_f32 v[164:165], v[118:119], v[148:149], v[164:165]
	s_waitcnt lgkmcnt(2)
	v_pk_fma_f32 v[162:163], v[100:101], v[150:151], v[162:163]
	v_pk_fma_f32 v[164:165], v[116:117], v[150:151], v[164:165]
	v_pk_fma_f32 v[162:163], v[98:99], v[152:153], v[162:163]
	v_pk_fma_f32 v[164:165], v[114:115], v[152:153], v[164:165]
	s_waitcnt lgkmcnt(1)
	v_pk_fma_f32 v[162:163], v[96:97], v[154:155], v[162:163]
	v_pk_fma_f32 v[164:165], v[112:113], v[154:155], v[164:165]
	v_pk_fma_f32 v[162:163], v[94:95], v[156:157], v[162:163]
	v_pk_fma_f32 v[164:165], v[110:111], v[156:157], v[164:165]
	s_waitcnt lgkmcnt(0)
	v_pk_fma_f32 v[162:163], v[92:93], v[158:159], v[162:163]
	v_pk_fma_f32 v[164:165], v[108:109], v[158:159], v[164:165]
	v_pk_fma_f32 v[162:163], v[90:91], v[160:161], v[162:163]
	v_pk_fma_f32 v[164:165], v[106:107], v[160:161], v[164:165]
	v_add_f32_e32 v90, v162, v163
	v_add_f32_e32 v91, v164, v165
	v_cndmask_b32_e64 v93, v178, v221, s[8:9]
	v_mov_b32_e32 v94, v93
	s_nop 1
	v_permlane32_swap_b32_e32 v93, v94
	v_cndmask_b32_e64 v93, v93, v94, s[8:9]
	v_cndmask_b32_e64 v94, v180, v223, s[8:9]
	v_mov_b32_e32 v95, v94
	s_nop 1
	v_permlane32_swap_b32_e32 v94, v95
	v_cndmask_b32_e64 v94, v94, v95, s[8:9]
	v_cndmask_b32_e64 v95, v182, v225, s[8:9]
	v_mov_b32_e32 v96, v95
	s_nop 1
	v_permlane32_swap_b32_e32 v95, v96
	v_cndmask_b32_e64 v95, v95, v96, s[8:9]
	v_cndmask_b32_e64 v96, v184, v227, s[8:9]
	v_mov_b32_e32 v97, v96
	s_nop 1
	v_permlane32_swap_b32_e32 v96, v97
	v_cndmask_b32_e64 v96, v96, v97, s[8:9]
	v_cndmask_b32_e64 v97, v186, v229, s[8:9]
	v_mov_b32_e32 v98, v97
	s_nop 1
	v_permlane32_swap_b32_e32 v97, v98
	v_cndmask_b32_e64 v97, v97, v98, s[8:9]
	v_cndmask_b32_e64 v98, v188, v231, s[8:9]
	v_mov_b32_e32 v99, v98
	s_nop 1
	v_permlane32_swap_b32_e32 v98, v99
	v_cndmask_b32_e64 v98, v98, v99, s[8:9]
	v_cndmask_b32_e64 v99, v190, v233, s[8:9]
	v_mov_b32_e32 v100, v99
	s_nop 1
	v_permlane32_swap_b32_e32 v99, v100
	v_cndmask_b32_e64 v99, v99, v100, s[8:9]
	v_cndmask_b32_e64 v100, v192, v235, s[8:9]
	v_mov_b32_e32 v101, v100
	s_nop 1
	v_permlane32_swap_b32_e32 v100, v101
	v_cndmask_b32_e64 v100, v100, v101, s[8:9]
	v_cndmask_b32_e64 v101, v194, v237, s[8:9]
	v_mov_b32_e32 v102, v101
	s_nop 1
	v_permlane32_swap_b32_e32 v101, v102
	v_cndmask_b32_e64 v101, v101, v102, s[8:9]
	v_cndmask_b32_e64 v102, v196, v239, s[8:9]
	v_mov_b32_e32 v103, v102
	s_nop 1
	v_permlane32_swap_b32_e32 v102, v103
	v_cndmask_b32_e64 v102, v102, v103, s[8:9]
	v_cndmask_b32_e64 v103, v198, v241, s[8:9]
	v_cndmask_b32_e64 v92, v221, v178, s[8:9]
	v_mov_b32_e32 v104, v103
	v_add_f32_e32 v92, v92, v93
	v_cndmask_b32_e64 v93, v223, v180, s[8:9]
	v_permlane32_swap_b32_e32 v103, v104
	v_add_f32_e32 v93, v93, v94
	v_cndmask_b32_e64 v94, v225, v182, s[8:9]
	v_cndmask_b32_e64 v103, v103, v104, s[8:9]
	v_cndmask_b32_e64 v104, v208, v243, s[8:9]
	v_add_f32_e32 v94, v94, v95
	v_cndmask_b32_e64 v95, v227, v184, s[8:9]
	v_mov_b32_e32 v105, v104
	v_add_f32_e32 v95, v95, v96
	v_cndmask_b32_e64 v96, v229, v186, s[8:9]
	v_permlane32_swap_b32_e32 v104, v105
	v_add_f32_e32 v96, v96, v97
	v_cndmask_b32_e64 v97, v231, v188, s[8:9]
	v_cndmask_b32_e64 v104, v104, v105, s[8:9]
	v_cndmask_b32_e64 v105, v213, v245, s[8:9]
	v_add_f32_e32 v97, v97, v98
	v_cndmask_b32_e64 v98, v233, v190, s[8:9]
	v_mov_b32_e32 v106, v105
	v_add_f32_e32 v98, v98, v99
	v_cndmask_b32_e64 v99, v235, v192, s[8:9]
	v_permlane32_swap_b32_e32 v105, v106
	v_add_f32_e32 v99, v99, v100
	v_cndmask_b32_e64 v100, v237, v194, s[8:9]
	v_cndmask_b32_e64 v105, v105, v106, s[8:9]
	v_cndmask_b32_e64 v106, v215, v212, s[8:9]
	v_add_f32_e32 v100, v100, v101
	v_cndmask_b32_e64 v101, v239, v196, s[8:9]
	v_mov_b32_e32 v107, v106
	v_add_f32_e32 v101, v101, v102
	v_cndmask_b32_e64 v102, v241, v198, s[8:9]
	v_permlane32_swap_b32_e32 v106, v107
	v_add_f32_e32 v102, v102, v103
	v_cndmask_b32_e64 v103, v243, v208, s[8:9]
	v_cndmask_b32_e64 v106, v106, v107, s[8:9]
	v_cndmask_b32_e64 v107, v216, v210, s[8:9]
	v_add_f32_e32 v103, v103, v104
	v_cndmask_b32_e64 v104, v245, v213, s[8:9]
	v_mov_b32_e32 v108, v107
	v_add_f32_e32 v104, v104, v105
	v_cndmask_b32_e64 v105, v212, v215, s[8:9]
	v_permlane32_swap_b32_e32 v107, v108
	v_add_f32_e32 v105, v105, v106
	v_cndmask_b32_e64 v106, v210, v216, s[8:9]
	v_cndmask_b32_e64 v107, v107, v108, s[8:9]
	v_add_f32_e32 v106, v106, v107
	v_cndmask_b32_e64 v107, v90, v218, s[8:9]
	v_cndmask_b32_e64 v90, v218, v90, s[8:9]
	v_mov_b32_e32 v108, v90
	s_nop 1
	v_permlane32_swap_b32_e32 v90, v108
	v_cndmask_b32_e64 v90, v90, v108, s[8:9]
	v_add_f32_e32 v90, v107, v90
	v_cndmask_b32_e64 v107, v100, v92, s[10:11]
	v_cndmask_b32_e64 v92, v92, v100, s[10:11]
	v_cndmask_b32_e64 v100, v101, v93, s[10:11]
	v_cndmask_b32_e64 v93, v93, v101, s[10:11]
	ds_swizzle_b32 v93, v93 offset:swizzle(SWAP,16)
	ds_swizzle_b32 v92, v92 offset:swizzle(SWAP,16)
	s_waitcnt lgkmcnt(1)
	v_add_f32_e32 v93, v100, v93
	v_cndmask_b32_e64 v100, v102, v94, s[10:11]
	v_cndmask_b32_e64 v94, v94, v102, s[10:11]
	ds_swizzle_b32 v94, v94 offset:swizzle(SWAP,16)
	s_waitcnt lgkmcnt(1)
	v_add_f32_e32 v92, v107, v92
	s_waitcnt lgkmcnt(0)
	v_add_f32_e32 v94, v100, v94
	v_cndmask_b32_e64 v100, v103, v95, s[10:11]
	v_cndmask_b32_e64 v95, v95, v103, s[10:11]
	ds_swizzle_b32 v95, v95 offset:swizzle(SWAP,16)
	s_waitcnt lgkmcnt(0)
	v_add_f32_e32 v95, v100, v95
	v_cndmask_b32_e64 v100, v104, v96, s[10:11]
	v_cndmask_b32_e64 v96, v96, v104, s[10:11]
	ds_swizzle_b32 v96, v96 offset:swizzle(SWAP,16)
	s_waitcnt lgkmcnt(0)
	v_add_f32_e32 v96, v100, v96
	v_cndmask_b32_e64 v100, v105, v97, s[10:11]
	v_cndmask_b32_e64 v97, v97, v105, s[10:11]
	ds_swizzle_b32 v97, v97 offset:swizzle(SWAP,16)
	s_waitcnt lgkmcnt(0)
	v_add_f32_e32 v97, v100, v97
	v_cndmask_b32_e64 v100, v106, v98, s[10:11]
	v_cndmask_b32_e64 v98, v98, v106, s[10:11]
	ds_swizzle_b32 v98, v98 offset:swizzle(SWAP,16)
	s_waitcnt lgkmcnt(0)
	v_add_f32_e32 v98, v100, v98
	v_cndmask_b32_e64 v100, v90, v99, s[10:11]
	v_cndmask_b32_e64 v90, v99, v90, s[10:11]
	v_cndmask_b32_e64 v99, v96, v92, s[12:13]
	v_cndmask_b32_e64 v92, v92, v96, s[12:13]
	v_cndmask_b32_e64 v96, v97, v93, s[12:13]
	v_cndmask_b32_e64 v93, v93, v97, s[12:13]
	ds_swizzle_b32 v93, v93 offset:swizzle(SWAP,8)
	ds_swizzle_b32 v90, v90 offset:swizzle(SWAP,16)
	ds_swizzle_b32 v92, v92 offset:swizzle(SWAP,8)
	s_waitcnt lgkmcnt(2)
	v_add_f32_e32 v93, v96, v93
	v_cndmask_b32_e64 v96, v98, v94, s[12:13]
	v_cndmask_b32_e64 v94, v94, v98, s[12:13]
	ds_swizzle_b32 v94, v94 offset:swizzle(SWAP,8)
	s_waitcnt lgkmcnt(2)
	v_add_f32_e32 v90, v100, v90
	s_waitcnt lgkmcnt(1)
	v_add_f32_e32 v92, v99, v92
	s_waitcnt lgkmcnt(0)
	v_add_f32_e32 v94, v96, v94
	v_cndmask_b32_e64 v96, v90, v95, s[12:13]
	v_cndmask_b32_e64 v90, v95, v90, s[12:13]
	ds_swizzle_b32 v90, v90 offset:swizzle(SWAP,8)
	v_cndmask_b32_e64 v95, v94, v92, s[14:15]
	v_cndmask_b32_e64 v92, v92, v94, s[14:15]
	ds_swizzle_b32 v92, v92 offset:swizzle(SWAP,4)
	s_waitcnt lgkmcnt(1)
	v_add_f32_e32 v90, v96, v90
	v_cndmask_b32_e64 v94, v90, v93, s[14:15]
	v_cndmask_b32_e64 v90, v93, v90, s[14:15]
	ds_swizzle_b32 v90, v90 offset:swizzle(SWAP,4)
	s_waitcnt lgkmcnt(1)
	v_add_f32_e32 v92, v95, v92
	s_waitcnt lgkmcnt(0)
	v_add_f32_e32 v90, v94, v90
	v_cndmask_b32_e64 v93, v90, v92, s[16:17]
	v_cndmask_b32_e64 v90, v92, v90, s[16:17]
	ds_swizzle_b32 v90, v90 offset:swizzle(SWAP,2)
	s_waitcnt lgkmcnt(0)
	v_add_f32_e32 v90, v93, v90
	v_cndmask_b32_e64 v93, v175, v217, s[8:9]
	v_mov_b32_e32 v94, v93
	s_nop 1
	v_permlane32_swap_b32_e32 v93, v94
	v_cndmask_b32_e64 v93, v93, v94, s[8:9]
	v_cndmask_b32_e64 v94, v176, v219, s[8:9]
	v_mov_b32_e32 v95, v94
	s_nop 1
	v_permlane32_swap_b32_e32 v94, v95
	v_cndmask_b32_e64 v94, v94, v95, s[8:9]
	v_cndmask_b32_e64 v95, v177, v220, s[8:9]
	v_mov_b32_e32 v96, v95
	s_nop 1
	v_permlane32_swap_b32_e32 v95, v96
	v_cndmask_b32_e64 v95, v95, v96, s[8:9]
	v_cndmask_b32_e64 v96, v179, v222, s[8:9]
	v_mov_b32_e32 v97, v96
	s_nop 1
	v_permlane32_swap_b32_e32 v96, v97
	v_cndmask_b32_e64 v96, v96, v97, s[8:9]
	v_cndmask_b32_e64 v97, v181, v224, s[8:9]
	v_mov_b32_e32 v98, v97
	s_nop 1
	v_permlane32_swap_b32_e32 v97, v98
	v_cndmask_b32_e64 v97, v97, v98, s[8:9]
	v_cndmask_b32_e64 v98, v183, v226, s[8:9]
	v_mov_b32_e32 v99, v98
	s_nop 1
	v_permlane32_swap_b32_e32 v98, v99
	v_cndmask_b32_e64 v98, v98, v99, s[8:9]
	v_cndmask_b32_e64 v99, v185, v228, s[8:9]
	v_mov_b32_e32 v100, v99
	s_nop 1
	v_permlane32_swap_b32_e32 v99, v100
	v_cndmask_b32_e64 v99, v99, v100, s[8:9]
	v_cndmask_b32_e64 v100, v187, v230, s[8:9]
	v_mov_b32_e32 v101, v100
	s_nop 1
	v_permlane32_swap_b32_e32 v100, v101
	v_cndmask_b32_e64 v100, v100, v101, s[8:9]
	v_cndmask_b32_e64 v101, v189, v232, s[8:9]
	ds_swizzle_b32 v92, v90 offset:swizzle(SWAP,1)
	v_mov_b32_e32 v102, v101
	s_nop 1
	v_permlane32_swap_b32_e32 v101, v102
	v_cndmask_b32_e64 v101, v101, v102, s[8:9]
	v_cndmask_b32_e64 v102, v191, v234, s[8:9]
	v_mov_b32_e32 v103, v102
	s_nop 1
	v_permlane32_swap_b32_e32 v102, v103
	s_waitcnt lgkmcnt(0)
	v_add_f32_e32 v90, v90, v92
	v_cndmask_b32_e64 v102, v102, v103, s[8:9]
	v_cndmask_b32_e64 v103, v193, v236, s[8:9]
	v_add_f32_e32 v92, v122, v90
	v_cndmask_b32_e64 v90, v217, v175, s[8:9]
	v_mov_b32_e32 v104, v103
	v_add_f32_e32 v90, v90, v93
	v_cndmask_b32_e64 v93, v219, v176, s[8:9]
	v_permlane32_swap_b32_e32 v103, v104
	v_add_f32_e32 v93, v93, v94
	v_cndmask_b32_e64 v94, v220, v177, s[8:9]
	v_cndmask_b32_e64 v103, v103, v104, s[8:9]
	v_cndmask_b32_e64 v104, v195, v238, s[8:9]
	v_add_f32_e32 v94, v94, v95
	v_cndmask_b32_e64 v95, v222, v179, s[8:9]
	v_mov_b32_e32 v105, v104
	v_add_f32_e32 v95, v95, v96
	v_cndmask_b32_e64 v96, v224, v181, s[8:9]
	v_permlane32_swap_b32_e32 v104, v105
	v_add_f32_e32 v96, v96, v97
	v_cndmask_b32_e64 v97, v226, v183, s[8:9]
	v_cndmask_b32_e64 v104, v104, v105, s[8:9]
	v_cndmask_b32_e64 v105, v197, v240, s[8:9]
	v_add_f32_e32 v97, v97, v98
	v_cndmask_b32_e64 v98, v228, v185, s[8:9]
	v_mov_b32_e32 v106, v105
	v_add_f32_e32 v98, v98, v99
	v_cndmask_b32_e64 v99, v230, v187, s[8:9]
	v_permlane32_swap_b32_e32 v105, v106
	v_add_f32_e32 v99, v99, v100
	v_cndmask_b32_e64 v100, v232, v189, s[8:9]
	v_cndmask_b32_e64 v105, v105, v106, s[8:9]
	v_cndmask_b32_e64 v106, v199, v242, s[8:9]
	v_add_f32_e32 v100, v100, v101
	v_cndmask_b32_e64 v101, v234, v191, s[8:9]
	v_mov_b32_e32 v107, v106
	v_add_f32_e32 v101, v101, v102
	v_cndmask_b32_e64 v102, v236, v193, s[8:9]
	v_permlane32_swap_b32_e32 v106, v107
	v_add_f32_e32 v102, v102, v103
	v_cndmask_b32_e64 v103, v238, v195, s[8:9]
	v_cndmask_b32_e64 v106, v106, v107, s[8:9]
	v_cndmask_b32_e64 v107, v209, v244, s[8:9]
	v_add_f32_e32 v103, v103, v104
	v_cndmask_b32_e64 v104, v240, v197, s[8:9]
	v_mov_b32_e32 v108, v107
	v_add_f32_e32 v104, v104, v105
	v_cndmask_b32_e64 v105, v242, v199, s[8:9]
	v_permlane32_swap_b32_e32 v107, v108
	v_add_f32_e32 v105, v105, v106
	v_cndmask_b32_e64 v106, v244, v209, s[8:9]
	v_cndmask_b32_e64 v107, v107, v108, s[8:9]
	v_add_f32_e32 v106, v106, v107
	v_cndmask_b32_e64 v107, v91, v214, s[8:9]
	v_cndmask_b32_e64 v91, v214, v91, s[8:9]
	v_mov_b32_e32 v108, v91
	s_nop 1
	v_permlane32_swap_b32_e32 v91, v108
	v_cndmask_b32_e64 v91, v91, v108, s[8:9]
	v_add_f32_e32 v91, v107, v91
	v_cndmask_b32_e64 v107, v100, v90, s[10:11]
	v_cndmask_b32_e64 v90, v90, v100, s[10:11]
	v_cndmask_b32_e64 v100, v101, v93, s[10:11]
	v_cndmask_b32_e64 v93, v93, v101, s[10:11]
	ds_swizzle_b32 v93, v93 offset:swizzle(SWAP,16)
	ds_swizzle_b32 v90, v90 offset:swizzle(SWAP,16)
	s_waitcnt lgkmcnt(1)
	v_add_f32_e32 v93, v100, v93
	v_cndmask_b32_e64 v100, v102, v94, s[10:11]
	v_cndmask_b32_e64 v94, v94, v102, s[10:11]
	ds_swizzle_b32 v94, v94 offset:swizzle(SWAP,16)
	s_waitcnt lgkmcnt(1)
	v_add_f32_e32 v90, v107, v90
	s_waitcnt lgkmcnt(0)
	v_add_f32_e32 v94, v100, v94
	v_cndmask_b32_e64 v100, v103, v95, s[10:11]
	v_cndmask_b32_e64 v95, v95, v103, s[10:11]
	ds_swizzle_b32 v95, v95 offset:swizzle(SWAP,16)
	s_waitcnt lgkmcnt(0)
	v_add_f32_e32 v95, v100, v95
	v_cndmask_b32_e64 v100, v104, v96, s[10:11]
	v_cndmask_b32_e64 v96, v96, v104, s[10:11]
	ds_swizzle_b32 v96, v96 offset:swizzle(SWAP,16)
	s_waitcnt lgkmcnt(0)
	v_add_f32_e32 v96, v100, v96
	v_cndmask_b32_e64 v100, v105, v97, s[10:11]
	v_cndmask_b32_e64 v97, v97, v105, s[10:11]
	ds_swizzle_b32 v97, v97 offset:swizzle(SWAP,16)
	s_waitcnt lgkmcnt(0)
	v_add_f32_e32 v97, v100, v97
	v_cndmask_b32_e64 v100, v106, v98, s[10:11]
	v_cndmask_b32_e64 v98, v98, v106, s[10:11]
	ds_swizzle_b32 v98, v98 offset:swizzle(SWAP,16)
	s_waitcnt lgkmcnt(0)
	v_add_f32_e32 v98, v100, v98
	v_cndmask_b32_e64 v100, v91, v99, s[10:11]
	v_cndmask_b32_e64 v91, v99, v91, s[10:11]
	v_cndmask_b32_e64 v99, v96, v90, s[12:13]
	v_cndmask_b32_e64 v90, v90, v96, s[12:13]
	v_cndmask_b32_e64 v96, v97, v93, s[12:13]
	v_cndmask_b32_e64 v93, v93, v97, s[12:13]
	ds_swizzle_b32 v93, v93 offset:swizzle(SWAP,8)
	ds_swizzle_b32 v91, v91 offset:swizzle(SWAP,16)
	ds_swizzle_b32 v90, v90 offset:swizzle(SWAP,8)
	s_waitcnt lgkmcnt(2)
	v_add_f32_e32 v93, v96, v93
	v_cndmask_b32_e64 v96, v98, v94, s[12:13]
	v_cndmask_b32_e64 v94, v94, v98, s[12:13]
	ds_swizzle_b32 v94, v94 offset:swizzle(SWAP,8)
	s_waitcnt lgkmcnt(2)
	v_add_f32_e32 v91, v100, v91
	s_waitcnt lgkmcnt(1)
	v_add_f32_e32 v90, v99, v90
	s_waitcnt lgkmcnt(0)
	v_add_f32_e32 v94, v96, v94
	v_cndmask_b32_e64 v96, v91, v95, s[12:13]
	v_cndmask_b32_e64 v91, v95, v91, s[12:13]
	ds_swizzle_b32 v91, v91 offset:swizzle(SWAP,8)
	v_cndmask_b32_e64 v95, v94, v90, s[14:15]
	v_cndmask_b32_e64 v90, v90, v94, s[14:15]
	ds_swizzle_b32 v90, v90 offset:swizzle(SWAP,4)
	s_waitcnt lgkmcnt(1)
	v_add_f32_e32 v91, v96, v91
	v_cndmask_b32_e64 v94, v91, v93, s[14:15]
	v_cndmask_b32_e64 v91, v93, v91, s[14:15]
	ds_swizzle_b32 v91, v91 offset:swizzle(SWAP,4)
	s_waitcnt lgkmcnt(1)
	v_add_f32_e32 v90, v95, v90
	s_waitcnt lgkmcnt(0)
	v_add_f32_e32 v91, v94, v91
	v_cndmask_b32_e64 v93, v91, v90, s[16:17]
	v_cndmask_b32_e64 v90, v90, v91, s[16:17]
	ds_swizzle_b32 v90, v90 offset:swizzle(SWAP,2)
	s_waitcnt lgkmcnt(0)
	v_add_f32_e32 v93, v93, v90
	ds_swizzle_b32 v94, v93 offset:swizzle(SWAP,1)
	s_and_saveexec_b64 s[84:85], s[18:19]
	ds_write_b32 v127, v92
	s_or_b64 exec, exec, s[84:85]
	s_waitcnt lgkmcnt(0)
	v_mov_b32_e32 v90, s4
	ds_read_b128 v[96:99], v90
	ds_read_b128 v[100:103], v90 offset:16
	ds_read_b128 v[104:107], v90 offset:32
	ds_read_b128 v[108:111], v90 offset:48
	s_waitcnt lgkmcnt(3)
	v_cmp_eq_f32_e64 s[84:85], v96, v92
	v_cmp_gt_f32_e32 vcc, v96, v92
	s_and_b64 s[84:85], s[84:85], s[20:21]
	s_or_b64 s[84:85], vcc, s[84:85]
	v_cndmask_b32_e64 v91, 0, 1, s[84:85]
	v_cmp_eq_f32_e64 s[84:85], v97, v92
	v_cmp_gt_f32_e32 vcc, v97, v92
	s_and_b64 s[84:85], s[84:85], s[22:23]
	s_or_b64 s[84:85], vcc, s[84:85]
	v_cndmask_b32_e64 v95, 0, 1, s[84:85]
	v_cmp_eq_f32_e64 s[84:85], v98, v92
	v_cmp_gt_f32_e32 vcc, v98, v92
	s_and_b64 s[84:85], s[84:85], s[24:25]
	s_or_b64 s[84:85], vcc, s[84:85]
	v_cndmask_b32_e64 v96, 0, 1, s[84:85]
	v_cmp_eq_f32_e64 s[84:85], v99, v92
	v_cmp_gt_f32_e32 vcc, v99, v92
	s_and_b64 s[84:85], s[84:85], s[26:27]
	s_or_b64 s[84:85], vcc, s[84:85]
	v_add3_u32 v91, v91, v95, v96
	v_cndmask_b32_e64 v95, 0, 1, s[84:85]
	s_waitcnt lgkmcnt(2)
	v_cmp_eq_f32_e64 s[84:85], v100, v92
	v_cmp_gt_f32_e32 vcc, v100, v92
	s_and_b64 s[84:85], s[84:85], s[28:29]
	s_or_b64 s[84:85], vcc, s[84:85]
	v_cndmask_b32_e64 v96, 0, 1, s[84:85]
	v_cmp_eq_f32_e64 s[84:85], v101, v92
	v_cmp_gt_f32_e32 vcc, v101, v92
	s_and_b64 s[84:85], s[84:85], s[30:31]
	s_or_b64 s[84:85], vcc, s[84:85]
	v_add3_u32 v91, v91, v95, v96
	v_cndmask_b32_e64 v95, 0, 1, s[84:85]
	v_cmp_eq_f32_e64 s[84:85], v102, v92
	v_cmp_gt_f32_e32 vcc, v102, v92
	s_and_b64 s[84:85], s[84:85], s[34:35]
	s_or_b64 s[84:85], vcc, s[84:85]
	v_cndmask_b32_e64 v96, 0, 1, s[84:85]
	v_cmp_eq_f32_e64 s[84:85], v103, v92
	v_cmp_gt_f32_e32 vcc, v103, v92
	s_and_b64 s[84:85], s[84:85], s[38:39]
	s_or_b64 s[84:85], vcc, s[84:85]
	v_add3_u32 v91, v91, v95, v96
	v_cndmask_b32_e64 v95, 0, 1, s[84:85]
	s_waitcnt lgkmcnt(1)
	v_cmp_eq_f32_e64 s[84:85], v104, v92
	v_cmp_gt_f32_e32 vcc, v104, v92
	s_and_b64 s[84:85], s[84:85], s[40:41]
	s_or_b64 s[84:85], vcc, s[84:85]
	v_cndmask_b32_e64 v96, 0, 1, s[84:85]
	v_cmp_eq_f32_e64 s[84:85], v105, v92
	v_cmp_gt_f32_e32 vcc, v105, v92
	s_and_b64 s[84:85], s[84:85], s[42:43]
	s_or_b64 s[84:85], vcc, s[84:85]
	v_add3_u32 v91, v91, v95, v96
	v_cndmask_b32_e64 v95, 0, 1, s[84:85]
	v_cmp_eq_f32_e64 s[84:85], v106, v92
	v_cmp_gt_f32_e32 vcc, v106, v92
	s_and_b64 s[84:85], s[84:85], s[44:45]
	s_or_b64 s[84:85], vcc, s[84:85]
	v_cndmask_b32_e64 v96, 0, 1, s[84:85]
	v_cmp_eq_f32_e64 s[84:85], v107, v92
	v_cmp_gt_f32_e32 vcc, v107, v92
	s_and_b64 s[84:85], s[84:85], s[46:47]
	s_or_b64 s[84:85], vcc, s[84:85]
	v_add3_u32 v91, v91, v95, v96
	v_cndmask_b32_e64 v95, 0, 1, s[84:85]
	s_waitcnt lgkmcnt(0)
	v_cmp_eq_f32_e64 s[84:85], v108, v92
	v_cmp_gt_f32_e32 vcc, v108, v92
	s_and_b64 s[84:85], s[84:85], s[48:49]
	s_or_b64 s[84:85], vcc, s[84:85]
	v_cndmask_b32_e64 v96, 0, 1, s[84:85]
	v_cmp_eq_f32_e64 s[84:85], v109, v92
	v_cmp_gt_f32_e32 vcc, v109, v92
	s_and_b64 s[84:85], s[84:85], s[50:51]
	s_or_b64 s[84:85], vcc, s[84:85]
	v_add3_u32 v91, v91, v95, v96
	v_cndmask_b32_e64 v95, 0, 1, s[84:85]
	v_cmp_eq_f32_e64 s[84:85], v110, v92
	v_cmp_gt_f32_e32 vcc, v110, v92
	s_and_b64 s[84:85], s[84:85], s[86:87]
	s_or_b64 s[84:85], vcc, s[84:85]
	v_cndmask_b32_e64 v96, 0, 1, s[84:85]
	v_add3_u32 v91, v91, v95, v96
	ds_read_b128 v[96:99], v90 offset:64
	ds_read_b128 v[100:103], v90 offset:80
	v_cmp_eq_f32_e64 s[84:85], v111, v92
	v_cmp_gt_f32_e32 vcc, v111, v92
	s_and_b64 s[84:85], s[84:85], s[52:53]
	s_or_b64 s[84:85], vcc, s[84:85]
	v_cndmask_b32_e64 v95, 0, 1, s[84:85]
	s_waitcnt lgkmcnt(1)
	v_cmp_eq_f32_e64 s[84:85], v96, v92
	v_cmp_gt_f32_e32 vcc, v96, v92
	s_and_b64 s[84:85], s[84:85], s[54:55]
	s_or_b64 s[84:85], vcc, s[84:85]
	v_cndmask_b32_e64 v96, 0, 1, s[84:85]
	v_cmp_eq_f32_e64 s[84:85], v97, v92
	v_cmp_gt_f32_e32 vcc, v97, v92
	s_and_b64 s[84:85], s[84:85], s[56:57]
	s_or_b64 s[84:85], vcc, s[84:85]
	v_add3_u32 v91, v91, v95, v96
	v_cndmask_b32_e64 v95, 0, 1, s[84:85]
	v_cmp_eq_f32_e64 s[84:85], v98, v92
	v_cmp_gt_f32_e32 vcc, v98, v92
	s_and_b64 s[84:85], s[84:85], s[58:59]
	s_or_b64 s[84:85], vcc, s[84:85]
	v_cndmask_b32_e64 v96, 0, 1, s[84:85]
	v_cmp_eq_f32_e64 s[84:85], v99, v92
	v_cmp_gt_f32_e32 vcc, v99, v92
	s_and_b64 s[84:85], s[84:85], s[60:61]
	s_or_b64 s[84:85], vcc, s[84:85]
	v_add3_u32 v91, v91, v95, v96
	v_cndmask_b32_e64 v95, 0, 1, s[84:85]
	s_waitcnt lgkmcnt(0)
	v_cmp_eq_f32_e64 s[84:85], v100, v92
	v_cmp_gt_f32_e32 vcc, v100, v92
	s_and_b64 s[84:85], s[84:85], s[62:63]
	s_or_b64 s[84:85], vcc, s[84:85]
	v_cndmask_b32_e64 v96, 0, 1, s[84:85]
	v_cmp_eq_f32_e64 s[84:85], v101, v92
	v_cmp_gt_f32_e32 vcc, v101, v92
	s_and_b64 s[84:85], s[84:85], s[64:65]
	s_or_b64 s[84:85], vcc, s[84:85]
	v_add3_u32 v91, v91, v95, v96
	v_cndmask_b32_e64 v95, 0, 1, s[84:85]
	v_cmp_eq_f32_e64 s[84:85], v102, v92
	v_cmp_gt_f32_e32 vcc, v102, v92
	s_and_b64 s[84:85], s[84:85], s[66:67]
	s_or_b64 s[84:85], vcc, s[84:85]
	v_cndmask_b32_e64 v96, 0, 1, s[84:85]
	v_add3_u32 v91, v91, v95, v96
	ds_read_b128 v[96:99], v90 offset:96
	v_cmp_eq_f32_e64 s[84:85], v103, v92
	v_cmp_gt_f32_e32 vcc, v103, v92
	s_and_b64 s[84:85], s[84:85], s[68:69]
	s_or_b64 s[84:85], vcc, s[84:85]
	v_cndmask_b32_e64 v95, 0, 1, s[84:85]
	ds_read_b128 v[100:103], v90 offset:112
	s_waitcnt lgkmcnt(1)
	v_cmp_eq_f32_e64 s[84:85], v96, v92
	v_cmp_gt_f32_e32 vcc, v96, v92
	s_and_b64 s[84:85], s[84:85], s[70:71]
	s_or_b64 s[84:85], vcc, s[84:85]
	v_cndmask_b32_e64 v90, 0, 1, s[84:85]
	v_cmp_eq_f32_e64 s[84:85], v97, v92
	v_cmp_gt_f32_e32 vcc, v97, v92
	s_and_b64 s[84:85], s[84:85], s[72:73]
	s_or_b64 s[84:85], vcc, s[84:85]
	v_cndmask_b32_e64 v96, 0, 1, s[84:85]
	v_cmp_eq_f32_e64 s[84:85], v98, v92
	v_cmp_gt_f32_e32 vcc, v98, v92
	s_and_b64 s[84:85], s[84:85], s[74:75]
	s_or_b64 s[84:85], vcc, s[84:85]
	v_cndmask_b32_e64 v97, 0, 1, s[84:85]
	v_cmp_eq_f32_e64 s[84:85], v99, v92
	v_cmp_gt_f32_e32 vcc, v99, v92
	s_and_b64 s[84:85], s[84:85], s[76:77]
	s_or_b64 s[84:85], vcc, s[84:85]
	v_cndmask_b32_e64 v98, 0, 1, s[84:85]
	s_waitcnt lgkmcnt(0)
	v_cmp_eq_f32_e64 s[84:85], v100, v92
	v_cmp_gt_f32_e32 vcc, v100, v92
	s_and_b64 s[84:85], s[84:85], s[78:79]
	s_or_b64 s[84:85], vcc, s[84:85]
	v_cndmask_b32_e64 v99, 0, 1, s[84:85]
	v_cmp_eq_f32_e64 s[84:85], v101, v92
	v_cmp_gt_f32_e32 vcc, v101, v92
	s_and_b64 s[84:85], s[84:85], s[80:81]
	s_or_b64 s[84:85], vcc, s[84:85]
	v_cndmask_b32_e64 v100, 0, 1, s[84:85]
	v_cmp_eq_f32_e64 s[84:85], v102, v92
	v_cmp_gt_f32_e32 vcc, v102, v92
	s_and_b64 s[84:85], s[82:83], s[84:85]
	s_or_b64 s[84:85], vcc, s[84:85]
	v_cmp_gt_f32_e32 vcc, v103, v92
	v_cndmask_b32_e64 v101, 0, 1, s[84:85]
	s_nop 0
	v_addc_co_u32_e32 v91, vcc, v91, v95, vcc
	v_add_u32_e32 v90, v91, v90
	v_add3_u32 v90, v90, v96, v97
	v_add3_u32 v90, v90, v98, v99
	v_add3_u32 v90, v90, v100, v101
	v_cmp_gt_u32_e32 vcc, 4, v90
	s_and_b64 vcc, s[0:1], vcc
	s_and_saveexec_b64 s[84:85], vcc
	v_lshl_add_u32 v91, v90, 2, s4
	ds_write_b32 v91, v92 offset:128
	s_or_b64 exec, exec, s[84:85]
	s_waitcnt lgkmcnt(0)
	s_and_saveexec_b64 s[84:85], vcc
	s_cbranch_execz .LBB0_773
	v_mov_b32_e32 v91, s4
	ds_read_b128 v[96:99], v91 offset:128
	s_waitcnt lgkmcnt(0)
	v_sub_f32_e32 v91, v97, v96
	v_sub_f32_e32 v95, v98, v96
	v_mul_f32_e32 v91, 0x3fb8aa3b, v91
	v_sub_f32_e32 v97, v99, v96
	v_mul_f32_e32 v95, 0x3fb8aa3b, v95
	v_exp_f32_e32 v91, v91
	v_mul_f32_e32 v97, 0x3fb8aa3b, v97
	v_exp_f32_e32 v95, v95
	v_exp_f32_e32 v97, v97
	v_add_f32_e32 v91, 1.0, v91
	v_sub_f32_e32 v92, v92, v96
	v_add_f32_e32 v91, v95, v91
	v_add_f32_e32 v91, v97, v91
	v_div_scale_f32 v95, s[92:93], v91, v91, 1.0
	v_rcp_f32_e32 v97, v95
	v_div_scale_f32 v98, vcc, 1.0, v91, 1.0
	s_lshl_b64 s[92:93], s[96:97], 4
	v_fma_f32 v99, -v95, v97, 1.0
	v_fmac_f32_e32 v97, v99, v97
	v_mul_f32_e32 v99, v98, v97
	v_fma_f32 v100, -v95, v99, v98
	v_fmac_f32_e32 v99, v100, v97
	v_fma_f32 v95, -v95, v99, v98
	v_div_fmas_f32 v95, v95, v97, v99
	v_div_fixup_f32 v95, v95, v91, 1.0
	v_mov_b32_e32 v91, v201
	v_lshlrev_b64 v[90:91], 2, v[90:91]
	v_mul_f32_e32 v92, 0x3fb8aa3b, v92
	v_or_b32_e32 v91, s93, v91
	v_exp_f32_e32 v92, v92
	v_or_b32_e32 v90, s92, v90
	v_readlane_b32 s92, v254, 45
	v_readlane_b32 s93, v254, 46
	v_mul_f32_e32 v92, v92, v95
	s_nop 0
	v_lshl_add_u64 v[96:97], s[92:93], 0, v[90:91]
	v_readlane_b32 s92, v254, 43
	v_readlane_b32 s93, v254, 44
	global_store_dword v[96:97], v126, off
	s_nop 0
	v_lshl_add_u64 v[90:91], s[92:93], 0, v[90:91]
	global_store_dword v[90:91], v92, off
	v_mov_b32_e32 v90, 1
	ds_add_u32 v128, v90
